# plus topk half-merge lane exchange via permlane32 self-swap and DPP reductions in ssm_finish GLU
# speedup vs baseline: 1.0053x; 1.0053x over previous
.LBB0_704:
	v_cndmask_b32_e64 v0, 0, 1, s[6:7]
	s_lshl_b32 s36, s8, 8
	v_cmp_ne_u32_e32 vcc, 1, v0
	v_lshl_add_u64 v[0:1], v[178:179], 0, s[36:37]
	global_load_dwordx4 v[44:47], v[0:1], off
	global_load_dwordx4 v[40:43], v[0:1], off offset:32
	global_load_dwordx4 v[36:39], v[0:1], off offset:64
	global_load_dwordx4 v[32:35], v[0:1], off offset:96
	global_load_dwordx4 v[28:31], v[0:1], off offset:128
	global_load_dwordx4 v[24:27], v[0:1], off offset:160
	global_load_dwordx4 v[20:23], v[0:1], off offset:192
	global_load_dwordx4 v[16:19], v[0:1], off offset:224
	v_lshl_or_b32 v180, s8, 7, v209
	v_ashrrev_i32_e32 v181, 31, v180
	v_lshlrev_b64 v[0:1], 8, v[180:181]
	v_lshl_add_u64 v[60:61], v[64:65], 0, v[0:1]
	global_load_dwordx4 v[0:3], v[60:61], off
	global_load_dwordx4 v[48:51], v[60:61], off offset:32
	global_load_dwordx4 v[52:55], v[60:61], off offset:64
	global_load_dwordx4 v[56:59], v[60:61], off offset:96
	s_nop 15
	s_nop 15
	s_waitcnt vmcnt(0)
	v_mfma_f32_32x32x16_bf16 v[0:15], v[0:3], v[44:47], 0
	v_mfma_f32_32x32x16_bf16 v[0:15], v[48:51], v[40:43], v[0:15]
	v_mfma_f32_32x32x16_bf16 v[0:15], v[52:55], v[36:39], v[0:15]
	v_mfma_f32_32x32x16_bf16 v[0:15], v[56:59], v[32:35], v[0:15]
	s_nop 15
	s_nop 15
	global_load_dwordx4 v[48:51], v[60:61], off offset:128
	global_load_dwordx4 v[52:55], v[60:61], off offset:160
	global_load_dwordx4 v[56:59], v[60:61], off offset:192
	s_nop 0
	global_load_dwordx4 v[60:63], v[60:61], off offset:224
	s_nop 15
	s_nop 15
	s_waitcnt vmcnt(3)
	v_mfma_f32_32x32x16_bf16 v[0:15], v[48:51], v[28:31], v[0:15]
	s_waitcnt vmcnt(2)
	v_mfma_f32_32x32x16_bf16 v[0:15], v[52:55], v[24:27], v[0:15]
	s_waitcnt vmcnt(1)
	v_mfma_f32_32x32x16_bf16 v[0:15], v[56:59], v[20:23], v[0:15]
	s_waitcnt vmcnt(0)
	v_mfma_f32_32x32x16_bf16 v[0:15], v[60:63], v[16:19], v[0:15]
	s_nop 15
	s_nop 15
	v_or_b32_e32 v49, 1, v66
	v_xor_b32_e32 v51, 0x7e, v66
	s_nop 9
	v_cmp_gt_i32_e64 s[6:7], 0, v1
	v_xor_b32_e32 v48, 0x7f, v66
	v_and_b32_e32 v1, 0xffffff80, v1
	v_cndmask_b32_e64 v49, v51, v49, s[6:7]
	v_cmp_gt_i32_e64 s[6:7], 0, v0
	v_and_b32_e32 v0, 0xffffff80, v0
	v_or_b32_e32 v210, v49, v1
	v_cndmask_b32_e64 v48, v48, v66, s[6:7]
	v_or_b32_e32 v211, v48, v0
	v_or_b32_e32 v48, 32, v180
	v_ashrrev_i32_e32 v49, 31, v48
	v_lshlrev_b64 v[48:49], 8, v[48:49]
	v_lshl_add_u64 v[182:183], v[64:65], 0, v[48:49]
	global_load_dwordx4 v[60:63], v[182:183], off
	global_load_dwordx4 v[56:59], v[182:183], off offset:32
	global_load_dwordx4 v[52:55], v[182:183], off offset:64
	global_load_dwordx4 v[48:51], v[182:183], off offset:96
	v_or_b32_e32 v1, 3, v66
	v_xor_b32_e32 v173, 0x7c, v66
	v_cmp_gt_i32_e64 s[6:7], 0, v3
	v_or_b32_e32 v0, 2, v66
	v_xor_b32_e32 v190, 0x7d, v66
	v_cndmask_b32_e64 v1, v173, v1, s[6:7]
	v_cmp_gt_i32_e64 s[6:7], 0, v2
	v_and_b32_e32 v3, 0xffffff80, v3
	v_and_b32_e32 v2, 0xffffff80, v2
	v_cndmask_b32_e64 v0, v190, v0, s[6:7]
	v_or_b32_e32 v173, v1, v3
	v_or_b32_e32 v1, 9, v66
	v_xor_b32_e32 v3, 0x76, v66
	v_cmp_gt_i32_e64 s[6:7], 0, v5
	v_or_b32_e32 v212, v0, v2
	v_or_b32_e32 v0, 8, v66
	v_cndmask_b32_e64 v1, v3, v1, s[6:7]
	v_xor_b32_e32 v2, 0x77, v66
	v_cmp_gt_i32_e64 s[6:7], 0, v4
	v_and_b32_e32 v3, 0xffffff80, v4
	s_nop 0
	v_cndmask_b32_e64 v0, v2, v0, s[6:7]
	v_and_b32_e32 v2, 0xffffff80, v5
	v_or_b32_e32 v213, v1, v2
	v_or_b32_e32 v214, v0, v3
	v_or_b32_e32 v1, 11, v66
	v_xor_b32_e32 v3, 0x74, v66
	v_cmp_gt_i32_e64 s[6:7], 0, v7
	v_or_b32_e32 v0, 10, v66
	v_xor_b32_e32 v2, 0x75, v66
	v_cndmask_b32_e64 v1, v3, v1, s[6:7]
	v_cmp_gt_i32_e64 s[6:7], 0, v6
	v_and_b32_e32 v3, 0xffffff80, v6
	s_nop 0
	v_cndmask_b32_e64 v0, v2, v0, s[6:7]
	v_and_b32_e32 v2, 0xffffff80, v7
	v_or_b32_e32 v215, v1, v2
	v_or_b32_e32 v216, v0, v3
	v_or_b32_e32 v1, 17, v66
	v_xor_b32_e32 v3, 0x6e, v66
	v_cmp_gt_i32_e64 s[6:7], 0, v9
	v_or_b32_e32 v0, 16, v66
	v_xor_b32_e32 v2, 0x6f, v66
	v_cndmask_b32_e64 v1, v3, v1, s[6:7]
	v_cmp_gt_i32_e64 s[6:7], 0, v8
	v_and_b32_e32 v3, 0xffffff80, v8
	s_nop 0
	v_cndmask_b32_e64 v0, v2, v0, s[6:7]
	v_and_b32_e32 v2, 0xffffff80, v9
	v_or_b32_e32 v217, v1, v2
	v_or_b32_e32 v218, v0, v3
	v_or_b32_e32 v1, 19, v66
	v_xor_b32_e32 v3, 0x6c, v66
	v_cmp_gt_i32_e64 s[6:7], 0, v11
	v_or_b32_e32 v0, 18, v66
	v_xor_b32_e32 v2, 0x6d, v66
	v_cndmask_b32_e64 v1, v3, v1, s[6:7]
	v_cmp_gt_i32_e64 s[6:7], 0, v10
	v_and_b32_e32 v3, 0xffffff80, v10
	s_nop 0
	v_cndmask_b32_e64 v0, v2, v0, s[6:7]
	v_and_b32_e32 v2, 0xffffff80, v11
	v_or_b32_e32 v219, v1, v2
	v_or_b32_e32 v220, v0, v3
	v_or_b32_e32 v1, 25, v66
	v_xor_b32_e32 v3, 0x66, v66
	v_cmp_gt_i32_e64 s[6:7], 0, v13
	v_or_b32_e32 v0, 24, v66
	v_xor_b32_e32 v2, 0x67, v66
	v_cndmask_b32_e64 v1, v3, v1, s[6:7]
	v_cmp_gt_i32_e64 s[6:7], 0, v12
	v_and_b32_e32 v3, 0xffffff80, v12
	s_nop 0
	v_cndmask_b32_e64 v0, v2, v0, s[6:7]
	v_and_b32_e32 v2, 0xffffff80, v13
	v_or_b32_e32 v221, v1, v2
	v_or_b32_e32 v1, 27, v66
	v_cmp_gt_i32_e64 s[6:7], 0, v15
	v_or_b32_e32 v222, v0, v3
	v_and_b32_e32 v2, 0xffffff80, v15
	v_cndmask_b32_e64 v0, v67, v1, s[6:7]
	v_cmp_gt_i32_e64 s[6:7], 0, v14
	v_and_b32_e32 v3, 0xffffff80, v14
	v_or_b32_e32 v223, v0, v2
	v_cndmask_b32_e64 v1, v70, v68, s[6:7]
	v_or_b32_e32 v224, v1, v3
	s_nop 15
	s_nop 15
	s_waitcnt vmcnt(3)
	v_mfma_f32_32x32x16_bf16 v[0:15], v[60:63], v[44:47], 0
	s_waitcnt vmcnt(2)
	v_mfma_f32_32x32x16_bf16 v[0:15], v[56:59], v[40:43], v[0:15]
	s_waitcnt vmcnt(1)
	v_mfma_f32_32x32x16_bf16 v[0:15], v[52:55], v[36:39], v[0:15]
	s_waitcnt vmcnt(0)
	v_mfma_f32_32x32x16_bf16 v[0:15], v[48:51], v[32:35], v[0:15]
	s_nop 15
	s_nop 15
	global_load_dwordx4 v[48:51], v[182:183], off offset:128
	global_load_dwordx4 v[52:55], v[182:183], off offset:160
	global_load_dwordx4 v[56:59], v[182:183], off offset:192
	global_load_dwordx4 v[60:63], v[182:183], off offset:224
	s_nop 15
	s_nop 15
	s_waitcnt vmcnt(3)
	v_mfma_f32_32x32x16_bf16 v[0:15], v[48:51], v[28:31], v[0:15]
	s_waitcnt vmcnt(2)
	v_mfma_f32_32x32x16_bf16 v[0:15], v[52:55], v[24:27], v[0:15]
	s_waitcnt vmcnt(1)
	v_mfma_f32_32x32x16_bf16 v[0:15], v[56:59], v[20:23], v[0:15]
	s_waitcnt vmcnt(0)
	v_mfma_f32_32x32x16_bf16 v[0:15], v[60:63], v[16:19], v[0:15]
	s_nop 15
	s_nop 15
	v_or_b32_e32 v48, 64, v180
	v_ashrrev_i32_e32 v49, 31, v48
	v_lshlrev_b64 v[48:49], 8, v[48:49]
	v_lshl_add_u64 v[182:183], v[64:65], 0, v[48:49]
	global_load_dwordx4 v[60:63], v[182:183], off
	global_load_dwordx4 v[56:59], v[182:183], off offset:32
	global_load_dwordx4 v[52:55], v[182:183], off offset:64
	global_load_dwordx4 v[48:51], v[182:183], off offset:96
	s_nop 3
	v_cmp_gt_i32_e64 s[6:7], 0, v1
	v_and_b32_e32 v1, 0xffffff80, v1
	s_nop 0
	v_cndmask_b32_e64 v181, v71, v69, s[6:7]
	v_cmp_gt_i32_e64 s[6:7], 0, v0
	v_and_b32_e32 v0, 0xffffff80, v0
	v_or_b32_e32 v225, v181, v1
	v_cndmask_b32_e64 v190, v74, v72, s[6:7]
	v_cmp_gt_i32_e64 s[6:7], 0, v3
	v_or_b32_e32 v226, v190, v0
	v_and_b32_e32 v3, 0xffffff80, v3
	v_cndmask_b32_e64 v0, v75, v73, s[6:7]
	v_cmp_gt_i32_e64 s[6:7], 0, v2
	v_and_b32_e32 v2, 0xffffff80, v2
	v_or_b32_e32 v227, v0, v3
	v_cndmask_b32_e64 v1, v78, v76, s[6:7]
	v_cmp_gt_i32_e64 s[6:7], 0, v5
	v_or_b32_e32 v228, v1, v2
	v_and_b32_e32 v2, 0xffffff80, v5
	v_cndmask_b32_e64 v0, v79, v77, s[6:7]
	v_cmp_gt_i32_e64 s[6:7], 0, v4
	v_and_b32_e32 v3, 0xffffff80, v4
	v_or_b32_e32 v229, v0, v2
	v_cndmask_b32_e64 v1, v82, v80, s[6:7]
	v_cmp_gt_i32_e64 s[6:7], 0, v7
	v_or_b32_e32 v230, v1, v3
	v_and_b32_e32 v2, 0xffffff80, v7
	v_cndmask_b32_e64 v0, v83, v81, s[6:7]
	v_cmp_gt_i32_e64 s[6:7], 0, v6
	v_and_b32_e32 v3, 0xffffff80, v6
	v_or_b32_e32 v231, v0, v2
	v_cndmask_b32_e64 v1, v86, v84, s[6:7]
	v_cmp_gt_i32_e64 s[6:7], 0, v9
	v_or_b32_e32 v232, v1, v3
	v_and_b32_e32 v2, 0xffffff80, v9
	v_cndmask_b32_e64 v0, v87, v85, s[6:7]
	v_cmp_gt_i32_e64 s[6:7], 0, v8
	v_and_b32_e32 v3, 0xffffff80, v8
	v_or_b32_e32 v233, v0, v2
	v_cndmask_b32_e64 v1, v90, v88, s[6:7]
	v_cmp_gt_i32_e64 s[6:7], 0, v11
	v_or_b32_e32 v234, v1, v3
	v_and_b32_e32 v2, 0xffffff80, v11
	v_cndmask_b32_e64 v0, v91, v89, s[6:7]
	v_cmp_gt_i32_e64 s[6:7], 0, v10
	v_and_b32_e32 v3, 0xffffff80, v10
	v_or_b32_e32 v235, v0, v2
	v_cndmask_b32_e64 v1, v94, v92, s[6:7]
	v_cmp_gt_i32_e64 s[6:7], 0, v13
	v_or_b32_e32 v236, v1, v3
	v_and_b32_e32 v2, 0xffffff80, v13
	v_cndmask_b32_e64 v0, v95, v93, s[6:7]
	v_cmp_gt_i32_e64 s[6:7], 0, v12
	v_and_b32_e32 v3, 0xffffff80, v12
	v_or_b32_e32 v237, v0, v2
	v_cndmask_b32_e64 v1, v98, v96, s[6:7]
	v_cmp_gt_i32_e64 s[6:7], 0, v15
	v_or_b32_e32 v238, v1, v3
	v_and_b32_e32 v2, 0xffffff80, v15
	v_cndmask_b32_e64 v0, v99, v97, s[6:7]
	v_cmp_gt_i32_e64 s[6:7], 0, v14
	v_and_b32_e32 v3, 0xffffff80, v14
	v_or_b32_e32 v239, v0, v2
	v_cndmask_b32_e64 v1, v102, v100, s[6:7]
	v_or_b32_e32 v240, v1, v3
	s_nop 15
	s_nop 15
	s_waitcnt vmcnt(3)
	v_mfma_f32_32x32x16_bf16 v[0:15], v[60:63], v[44:47], 0
	s_waitcnt vmcnt(2)
	v_mfma_f32_32x32x16_bf16 v[0:15], v[56:59], v[40:43], v[0:15]
	s_waitcnt vmcnt(1)
	v_mfma_f32_32x32x16_bf16 v[0:15], v[52:55], v[36:39], v[0:15]
	s_waitcnt vmcnt(0)
	v_mfma_f32_32x32x16_bf16 v[0:15], v[48:51], v[32:35], v[0:15]
	s_nop 15
	s_nop 15
	global_load_dwordx4 v[48:51], v[182:183], off offset:128
	global_load_dwordx4 v[52:55], v[182:183], off offset:160
	global_load_dwordx4 v[56:59], v[182:183], off offset:192
	global_load_dwordx4 v[60:63], v[182:183], off offset:224
	s_nop 15
	s_nop 15
	s_waitcnt vmcnt(3)
	v_mfma_f32_32x32x16_bf16 v[0:15], v[48:51], v[28:31], v[0:15]
	s_waitcnt vmcnt(2)
	v_mfma_f32_32x32x16_bf16 v[0:15], v[52:55], v[24:27], v[0:15]
	s_waitcnt vmcnt(1)
	v_mfma_f32_32x32x16_bf16 v[0:15], v[56:59], v[20:23], v[0:15]
	s_waitcnt vmcnt(0)
	v_mfma_f32_32x32x16_bf16 v[0:15], v[60:63], v[16:19], v[0:15]
	s_nop 15
	s_nop 15
	v_or_b32_e32 v48, 0x60, v180
	v_ashrrev_i32_e32 v49, 31, v48
	v_lshlrev_b64 v[48:49], 8, v[48:49]
	v_lshl_add_u64 v[180:181], v[64:65], 0, v[48:49]
	global_load_dwordx4 v[60:63], v[180:181], off
	global_load_dwordx4 v[56:59], v[180:181], off offset:32
	global_load_dwordx4 v[52:55], v[180:181], off offset:64
	global_load_dwordx4 v[48:51], v[180:181], off offset:96
	s_nop 3
	v_cmp_gt_i32_e64 s[6:7], 0, v1
	v_and_b32_e32 v1, 0xffffff80, v1
	s_nop 0
	v_cndmask_b32_e64 v182, v103, v101, s[6:7]
	v_cmp_gt_i32_e64 s[6:7], 0, v0
	v_and_b32_e32 v0, 0xffffff80, v0
	v_or_b32_e32 v182, v182, v1
	v_cndmask_b32_e64 v183, v106, v104, s[6:7]
	v_cmp_gt_i32_e64 s[6:7], 0, v3
	v_or_b32_e32 v183, v183, v0
	v_and_b32_e32 v3, 0xffffff80, v3
	v_cndmask_b32_e64 v0, v107, v105, s[6:7]
	v_cmp_gt_i32_e64 s[6:7], 0, v2
	v_and_b32_e32 v2, 0xffffff80, v2
	v_or_b32_e32 v241, v0, v3
	v_cndmask_b32_e64 v1, v110, v108, s[6:7]
	v_cmp_gt_i32_e64 s[6:7], 0, v5
	v_or_b32_e32 v242, v1, v2
	v_and_b32_e32 v2, 0xffffff80, v5
	v_cndmask_b32_e64 v0, v111, v109, s[6:7]
	v_cmp_gt_i32_e64 s[6:7], 0, v4
	v_and_b32_e32 v3, 0xffffff80, v4
	v_or_b32_e32 v243, v0, v2
	v_cndmask_b32_e64 v1, v114, v112, s[6:7]
	v_cmp_gt_i32_e64 s[6:7], 0, v7
	v_or_b32_e32 v244, v1, v3
	v_and_b32_e32 v2, 0xffffff80, v7
	v_cndmask_b32_e64 v0, v115, v113, s[6:7]
	v_cmp_gt_i32_e64 s[6:7], 0, v6
	v_and_b32_e32 v3, 0xffffff80, v6
	v_or_b32_e32 v245, v0, v2
	v_cndmask_b32_e64 v1, v118, v116, s[6:7]
	v_cmp_gt_i32_e64 s[6:7], 0, v9
	v_or_b32_e32 v246, v1, v3
	v_and_b32_e32 v2, 0xffffff80, v9
	v_cndmask_b32_e64 v0, v119, v117, s[6:7]
	v_cmp_gt_i32_e64 s[6:7], 0, v8
	v_and_b32_e32 v3, 0xffffff80, v8
	v_or_b32_e32 v247, v0, v2
	v_cndmask_b32_e64 v1, v122, v120, s[6:7]
	v_cmp_gt_i32_e64 s[6:7], 0, v11
	v_or_b32_e32 v248, v1, v3
	v_and_b32_e32 v2, 0xffffff80, v11
	v_cndmask_b32_e64 v0, v123, v121, s[6:7]
	v_cmp_gt_i32_e64 s[6:7], 0, v10
	v_and_b32_e32 v3, 0xffffff80, v10
	v_or_b32_e32 v249, v0, v2
	v_cndmask_b32_e64 v1, v126, v124, s[6:7]
	v_cmp_gt_i32_e64 s[6:7], 0, v13
	v_or_b32_e32 v250, v1, v3
	v_and_b32_e32 v2, 0xffffff80, v13
	v_cndmask_b32_e64 v0, v127, v125, s[6:7]
	v_cmp_gt_i32_e64 s[6:7], 0, v12
	v_and_b32_e32 v3, 0xffffff80, v12
	v_or_b32_e32 v251, v0, v2
	v_cndmask_b32_e64 v1, v130, v128, s[6:7]
	v_cmp_gt_i32_e64 s[6:7], 0, v15
	v_or_b32_e32 v252, v1, v3
	v_and_b32_e32 v2, 0xffffff80, v15
	v_cndmask_b32_e64 v0, v131, v129, s[6:7]
	v_cmp_gt_i32_e64 s[6:7], 0, v14
	v_and_b32_e32 v3, 0xffffff80, v14
	v_or_b32_e32 v190, v0, v2
	v_cndmask_b32_e64 v1, v134, v132, s[6:7]
	v_or_b32_e32 v195, v1, v3
	s_nop 15
	s_nop 15
	s_waitcnt vmcnt(3)
	v_mfma_f32_32x32x16_bf16 v[0:15], v[60:63], v[44:47], 0
	s_waitcnt vmcnt(2)
	v_mfma_f32_32x32x16_bf16 v[0:15], v[56:59], v[40:43], v[0:15]
	s_waitcnt vmcnt(1)
	v_mfma_f32_32x32x16_bf16 v[0:15], v[52:55], v[36:39], v[0:15]
	s_waitcnt vmcnt(0)
	v_mfma_f32_32x32x16_bf16 v[0:15], v[48:51], v[32:35], v[0:15]
	s_nop 15
	s_nop 15
	global_load_dwordx4 v[32:35], v[180:181], off offset:128
	global_load_dwordx4 v[36:39], v[180:181], off offset:160
	global_load_dwordx4 v[40:43], v[180:181], off offset:192
	global_load_dwordx4 v[44:47], v[180:181], off offset:224
	s_nop 15
	s_nop 15
	s_waitcnt vmcnt(3)
	v_mfma_f32_32x32x16_bf16 v[0:15], v[32:35], v[28:31], v[0:15]
	s_waitcnt vmcnt(2)
	v_mfma_f32_32x32x16_bf16 v[0:15], v[36:39], v[24:27], v[0:15]
	s_waitcnt vmcnt(1)
	v_mfma_f32_32x32x16_bf16 v[0:15], v[40:43], v[20:23], v[0:15]
	s_waitcnt vmcnt(0)
	v_mfma_f32_32x32x16_bf16 v[0:15], v[44:47], v[16:19], v[0:15]
	s_nop 15
	s_nop 15
	s_nop 11
	v_cmp_gt_i32_e64 s[6:7], 0, v1
	v_and_b32_e32 v1, 0xffffff80, v1
	v_and_b32_e32 v18, 0xffffff80, v0
	v_cndmask_b32_e64 v16, v135, v133, s[6:7]
	v_cmp_gt_i32_e64 s[6:7], 0, v0
	v_or_b32_e32 v0, v16, v1
	s_nop 0
	v_cndmask_b32_e64 v17, v138, v136, s[6:7]
	v_cmp_gt_i32_e64 s[6:7], 0, v3
	v_or_b32_e32 v1, v17, v18
	v_and_b32_e32 v3, 0xffffff80, v3
	v_cndmask_b32_e64 v16, v139, v137, s[6:7]
	v_cmp_gt_i32_e64 s[6:7], 0, v2
	v_and_b32_e32 v18, 0xffffff80, v2
	v_or_b32_e32 v2, v16, v3
	v_cndmask_b32_e64 v17, v142, v140, s[6:7]
	v_cmp_gt_i32_e64 s[6:7], 0, v5
	v_or_b32_e32 v3, v17, v18
	v_and_b32_e32 v5, 0xffffff80, v5
	v_cndmask_b32_e64 v16, v143, v141, s[6:7]
	v_cmp_gt_i32_e64 s[6:7], 0, v4
	v_and_b32_e32 v18, 0xffffff80, v4
	v_or_b32_e32 v4, v16, v5
	v_cndmask_b32_e64 v17, v154, v152, s[6:7]
	v_cmp_gt_i32_e64 s[6:7], 0, v7
	v_or_b32_e32 v5, v17, v18
	v_and_b32_e32 v7, 0xffffff80, v7
	v_cndmask_b32_e64 v16, v155, v153, s[6:7]
	v_cmp_gt_i32_e64 s[6:7], 0, v6
	v_and_b32_e32 v18, 0xffffff80, v6
	v_or_b32_e32 v6, v16, v7
	v_cndmask_b32_e64 v17, v158, v156, s[6:7]
	v_cmp_gt_i32_e64 s[6:7], 0, v9
	v_or_b32_e32 v7, v17, v18
	v_and_b32_e32 v9, 0xffffff80, v9
	v_cndmask_b32_e64 v16, v159, v157, s[6:7]
	v_cmp_gt_i32_e64 s[6:7], 0, v8
	v_and_b32_e32 v18, 0xffffff80, v8
	v_or_b32_e32 v8, v16, v9
	v_cndmask_b32_e64 v17, v162, v160, s[6:7]
	v_cmp_gt_i32_e64 s[6:7], 0, v11
	v_or_b32_e32 v9, v17, v18
	v_and_b32_e32 v11, 0xffffff80, v11
	v_cndmask_b32_e64 v16, v163, v161, s[6:7]
	v_cmp_gt_i32_e64 s[6:7], 0, v10
	v_and_b32_e32 v18, 0xffffff80, v10
	v_or_b32_e32 v10, v16, v11
	v_cndmask_b32_e64 v17, v166, v164, s[6:7]
	v_cmp_gt_i32_e64 s[6:7], 0, v13
	v_or_b32_e32 v11, v17, v18
	v_and_b32_e32 v13, 0xffffff80, v13
	v_cndmask_b32_e64 v16, v167, v165, s[6:7]
	v_cmp_gt_i32_e64 s[6:7], 0, v12
	v_and_b32_e32 v18, 0xffffff80, v12
	v_or_b32_e32 v12, v16, v13
	v_cndmask_b32_e64 v17, v170, v168, s[6:7]
	v_cmp_gt_i32_e64 s[6:7], 0, v15
	v_or_b32_e32 v16, v17, v18
	v_and_b32_e32 v15, 0xffffff80, v15
	v_cndmask_b32_e64 v13, v171, v169, s[6:7]
	v_cmp_gt_i32_e64 s[6:7], 0, v14
	v_and_b32_e32 v14, 0xffffff80, v14
	v_or_b32_e32 v25, v13, v15
	v_cndmask_b32_e64 v17, v174, v172, s[6:7]
	v_or_b32_e32 v28, v17, v14
	v_max_f32_e32 v13, v211, v210
	v_min_f32_e32 v14, v211, v210
	v_min_f32_e32 v15, v212, v173
	v_max_f32_e32 v17, v212, v173
	v_max_f32_e32 v18, v214, v213
	v_min_f32_e32 v19, v214, v213
	v_min_f32_e32 v20, v216, v215
	v_max_f32_e32 v21, v216, v215
	v_max_f32_e32 v22, v218, v217
	v_min_f32_e32 v23, v218, v217
	v_min_f32_e32 v24, v220, v219
	v_max_f32_e32 v26, v220, v219
	v_max_f32_e32 v27, v222, v221
	v_min_f32_e32 v29, v222, v221
	v_min_f32_e32 v30, v224, v223
	v_max_f32_e32 v31, v224, v223
	v_max_f32_e32 v32, v13, v15
	v_min_f32_e32 v13, v13, v15
	v_max_f32_e32 v15, v14, v17
	v_min_f32_e32 v14, v14, v17
	v_min_f32_e32 v17, v18, v20
	v_max_f32_e32 v18, v18, v20
	v_min_f32_e32 v20, v19, v21
	v_max_f32_e32 v19, v19, v21
	v_max_f32_e32 v21, v22, v24
	v_min_f32_e32 v22, v22, v24
	v_max_f32_e32 v24, v23, v26
	v_min_f32_e32 v23, v23, v26
	v_min_f32_e32 v26, v27, v30
	v_max_f32_e32 v27, v27, v30
	v_min_f32_e32 v30, v29, v31
	v_max_f32_e32 v29, v29, v31
	v_max_f32_e32 v31, v32, v15
	v_min_f32_e32 v15, v32, v15
	v_max_f32_e32 v32, v13, v14
	v_min_f32_e32 v13, v13, v14
	v_min_f32_e32 v14, v17, v20
	v_max_f32_e32 v17, v17, v20
	v_min_f32_e32 v20, v18, v19
	v_max_f32_e32 v18, v18, v19
	v_max_f32_e32 v19, v21, v24
	v_min_f32_e32 v21, v21, v24
	v_max_f32_e32 v24, v22, v23
	v_min_f32_e32 v22, v22, v23
	v_min_f32_e32 v23, v26, v30
	v_max_f32_e32 v26, v26, v30
	v_min_f32_e32 v30, v27, v29
	v_max_f32_e32 v27, v27, v29
	v_max_f32_e32 v29, v31, v14
	v_min_f32_e32 v14, v31, v14
	v_max_f32_e32 v31, v15, v17
	v_min_f32_e32 v15, v15, v17
	v_max_f32_e32 v17, v32, v20
	v_min_f32_e32 v20, v32, v20
	v_max_f32_e32 v32, v13, v18
	v_min_f32_e32 v13, v13, v18
	v_min_f32_e32 v18, v19, v23
	v_max_f32_e32 v19, v19, v23
	v_min_f32_e32 v23, v21, v26
	v_max_f32_e32 v21, v21, v26
	v_min_f32_e32 v26, v24, v30
	v_max_f32_e32 v24, v24, v30
	v_min_f32_e32 v30, v22, v27
	v_max_f32_e32 v22, v22, v27
	v_max_f32_e32 v27, v29, v17
	v_min_f32_e32 v17, v29, v17
	v_max_f32_e32 v29, v31, v32
	v_min_f32_e32 v31, v31, v32
	v_max_f32_e32 v32, v14, v20
	v_min_f32_e32 v14, v14, v20
	v_max_f32_e32 v20, v15, v13
	v_min_f32_e32 v13, v15, v13
	v_min_f32_e32 v15, v18, v26
	v_max_f32_e32 v18, v18, v26
	v_min_f32_e32 v26, v23, v30
	v_max_f32_e32 v23, v23, v30
	v_min_f32_e32 v30, v19, v24
	v_max_f32_e32 v19, v19, v24
	v_min_f32_e32 v24, v21, v22
	v_max_f32_e32 v21, v21, v22
	v_max_f32_e32 v22, v27, v29
	v_min_f32_e32 v27, v27, v29
	v_max_f32_e32 v29, v17, v31
	v_min_f32_e32 v17, v17, v31
	v_max_f32_e32 v31, v32, v20
	v_min_f32_e32 v20, v32, v20
	v_max_f32_e32 v32, v14, v13
	v_min_f32_e32 v13, v14, v13
	v_min_f32_e32 v14, v15, v26
	v_max_f32_e32 v15, v15, v26
	v_min_f32_e32 v26, v18, v23
	v_max_f32_e32 v18, v18, v23
	v_min_f32_e32 v23, v30, v24
	v_max_f32_e32 v24, v30, v24
	v_min_f32_e32 v30, v19, v21
	v_max_f32_e32 v19, v19, v21
	v_max_f32_e32 v21, v22, v14
	v_min_f32_e32 v14, v22, v14
	v_max_f32_e32 v22, v27, v15
	v_min_f32_e32 v15, v27, v15
	v_max_f32_e32 v27, v29, v26
	v_min_f32_e32 v26, v29, v26
	v_max_f32_e32 v29, v17, v18
	v_min_f32_e32 v17, v17, v18
	v_max_f32_e32 v18, v31, v23
	v_min_f32_e32 v23, v31, v23
	v_max_f32_e32 v31, v20, v24
	v_min_f32_e32 v20, v20, v24
	v_max_f32_e32 v24, v32, v30
	v_min_f32_e32 v30, v32, v30
	v_max_f32_e32 v32, v13, v19
	v_min_f32_e32 v13, v13, v19
	v_max_f32_e32 v19, v21, v18
	v_min_f32_e32 v18, v21, v18
	v_max_f32_e32 v21, v22, v31
	v_min_f32_e32 v22, v22, v31
	v_max_f32_e32 v31, v27, v24
	v_min_f32_e32 v24, v27, v24
	v_max_f32_e32 v27, v29, v32
	v_min_f32_e32 v29, v29, v32
	v_max_f32_e32 v32, v14, v23
	v_min_f32_e32 v14, v14, v23
	v_max_f32_e32 v23, v15, v20
	v_min_f32_e32 v15, v15, v20
	v_max_f32_e32 v20, v26, v30
	v_min_f32_e32 v26, v26, v30
	v_max_f32_e32 v30, v17, v13
	v_min_f32_e32 v13, v17, v13
	v_max_f32_e32 v17, v19, v31
	v_min_f32_e32 v19, v19, v31
	v_max_f32_e32 v33, v21, v27
	v_min_f32_e32 v21, v21, v27
	v_max_f32_e32 v34, v18, v24
	v_min_f32_e32 v18, v18, v24
	v_max_f32_e32 v24, v22, v29
	v_min_f32_e32 v22, v22, v29
	v_max_f32_e32 v35, v32, v20
	v_min_f32_e32 v32, v32, v20
	v_max_f32_e32 v20, v23, v30
	v_min_f32_e32 v36, v23, v30
	v_max_f32_e32 v37, v14, v26
	v_min_f32_e32 v38, v14, v26
	v_max_f32_e32 v14, v15, v13
	v_min_f32_e32 v13, v15, v13
	v_max_f32_e32 v31, v17, v33
	v_min_f32_e32 v29, v17, v33
	v_max_f32_e32 v30, v19, v21
	v_min_f32_e32 v26, v19, v21
	v_max_f32_e32 v27, v34, v24
	v_min_f32_e32 v23, v34, v24
	v_max_f32_e32 v24, v18, v22
	v_min_f32_e32 v21, v18, v22
	v_max_f32_e32 v22, v35, v20
	v_min_f32_e32 v19, v35, v20
	v_max_f32_e32 v20, v32, v36
	v_min_f32_e32 v17, v32, v36
	v_max_f32_e32 v18, v37, v14
	v_min_f32_e32 v14, v37, v14
	v_max_f32_e32 v15, v38, v13
	v_min_f32_e32 v13, v38, v13
	v_max_f32_e32 v32, v226, v225
	v_min_f32_e32 v33, v226, v225
	v_min_f32_e32 v34, v228, v227
	v_max_f32_e32 v35, v228, v227
	v_max_f32_e32 v36, v230, v229
	v_min_f32_e32 v37, v230, v229
	v_min_f32_e32 v38, v232, v231
	v_max_f32_e32 v39, v232, v231
	v_max_f32_e32 v40, v234, v233
	v_min_f32_e32 v41, v234, v233
	v_min_f32_e32 v42, v236, v235
	v_max_f32_e32 v43, v236, v235
	v_max_f32_e32 v44, v238, v237
	v_min_f32_e32 v45, v238, v237
	v_min_f32_e32 v46, v240, v239
	v_max_f32_e32 v47, v240, v239
	v_max_f32_e32 v48, v32, v34
	v_min_f32_e32 v32, v32, v34
	v_max_f32_e32 v34, v33, v35
	v_min_f32_e32 v33, v33, v35
	v_min_f32_e32 v35, v36, v38
	v_max_f32_e32 v36, v36, v38
	v_min_f32_e32 v38, v37, v39
	v_max_f32_e32 v37, v37, v39
	v_max_f32_e32 v39, v40, v42
	v_min_f32_e32 v40, v40, v42
	v_max_f32_e32 v42, v41, v43
	v_min_f32_e32 v41, v41, v43
	v_min_f32_e32 v43, v44, v46
	v_max_f32_e32 v44, v44, v46
	v_min_f32_e32 v46, v45, v47
	v_max_f32_e32 v45, v45, v47
	v_max_f32_e32 v47, v48, v34
	v_min_f32_e32 v34, v48, v34
	v_max_f32_e32 v48, v32, v33
	v_min_f32_e32 v32, v32, v33
	v_min_f32_e32 v33, v35, v38
	v_max_f32_e32 v35, v35, v38
	v_min_f32_e32 v38, v36, v37
	v_max_f32_e32 v36, v36, v37
	v_max_f32_e32 v37, v39, v42
	v_min_f32_e32 v39, v39, v42
	v_max_f32_e32 v42, v40, v41
	v_min_f32_e32 v40, v40, v41
	v_min_f32_e32 v41, v43, v46
	v_max_f32_e32 v43, v43, v46
	v_min_f32_e32 v46, v44, v45
	v_max_f32_e32 v44, v44, v45
	v_max_f32_e32 v45, v47, v33
	v_min_f32_e32 v33, v47, v33
	v_max_f32_e32 v47, v34, v35
	v_min_f32_e32 v34, v34, v35
	v_max_f32_e32 v35, v48, v38
	v_min_f32_e32 v38, v48, v38
	v_max_f32_e32 v48, v32, v36
	v_min_f32_e32 v32, v32, v36
	v_min_f32_e32 v36, v37, v41
	v_max_f32_e32 v37, v37, v41
	v_min_f32_e32 v41, v39, v43
	v_max_f32_e32 v39, v39, v43
	v_min_f32_e32 v43, v42, v46
	v_max_f32_e32 v42, v42, v46
	v_min_f32_e32 v46, v40, v44
	v_max_f32_e32 v40, v40, v44
	v_max_f32_e32 v44, v45, v35
	v_min_f32_e32 v35, v45, v35
	v_max_f32_e32 v45, v47, v48
	v_min_f32_e32 v47, v47, v48
	v_max_f32_e32 v48, v33, v38
	v_min_f32_e32 v33, v33, v38
	v_max_f32_e32 v38, v34, v32
	v_min_f32_e32 v32, v34, v32
	v_min_f32_e32 v34, v36, v43
	v_max_f32_e32 v36, v36, v43
	v_min_f32_e32 v43, v41, v46
	v_max_f32_e32 v41, v41, v46
	v_min_f32_e32 v46, v37, v42
	v_max_f32_e32 v37, v37, v42
	v_min_f32_e32 v42, v39, v40
	v_max_f32_e32 v39, v39, v40
	v_max_f32_e32 v40, v44, v45
	v_min_f32_e32 v44, v44, v45
	v_max_f32_e32 v45, v35, v47
	v_min_f32_e32 v35, v35, v47
	v_max_f32_e32 v47, v48, v38
	v_min_f32_e32 v38, v48, v38
	v_max_f32_e32 v48, v33, v32
	v_min_f32_e32 v32, v33, v32
	v_min_f32_e32 v33, v34, v43
	v_max_f32_e32 v34, v34, v43
	v_min_f32_e32 v43, v36, v41
	v_max_f32_e32 v36, v36, v41
	v_min_f32_e32 v41, v46, v42
	v_max_f32_e32 v42, v46, v42
	v_min_f32_e32 v46, v37, v39
	v_max_f32_e32 v37, v37, v39
	v_max_f32_e32 v39, v40, v33
	v_min_f32_e32 v33, v40, v33
	v_max_f32_e32 v40, v44, v34
	v_min_f32_e32 v34, v44, v34
	v_max_f32_e32 v44, v45, v43
	v_min_f32_e32 v43, v45, v43
	v_max_f32_e32 v45, v35, v36
	v_min_f32_e32 v35, v35, v36
	v_max_f32_e32 v36, v47, v41
	v_min_f32_e32 v41, v47, v41
	v_max_f32_e32 v47, v38, v42
	v_min_f32_e32 v38, v38, v42
	v_max_f32_e32 v42, v48, v46
	v_min_f32_e32 v46, v48, v46
	v_max_f32_e32 v48, v32, v37
	v_min_f32_e32 v32, v32, v37
	v_max_f32_e32 v37, v39, v36
	v_min_f32_e32 v36, v39, v36
	v_max_f32_e32 v39, v40, v47
	v_min_f32_e32 v40, v40, v47
	v_max_f32_e32 v47, v44, v42
	v_min_f32_e32 v42, v44, v42
	v_max_f32_e32 v44, v45, v48
	v_min_f32_e32 v45, v45, v48
	v_max_f32_e32 v48, v33, v41
	v_min_f32_e32 v33, v33, v41
	v_max_f32_e32 v41, v34, v38
	v_min_f32_e32 v34, v34, v38
	v_max_f32_e32 v38, v43, v46
	v_min_f32_e32 v43, v43, v46
	v_max_f32_e32 v46, v35, v32
	v_min_f32_e32 v32, v35, v32
	v_max_f32_e32 v35, v37, v47
	v_min_f32_e32 v37, v37, v47
	v_max_f32_e32 v47, v39, v44
	v_min_f32_e32 v39, v39, v44
	v_max_f32_e32 v44, v36, v42
	v_min_f32_e32 v42, v36, v42
	v_max_f32_e32 v49, v40, v45
	v_min_f32_e32 v40, v40, v45
	v_max_f32_e32 v45, v48, v38
	v_min_f32_e32 v48, v48, v38
	v_max_f32_e32 v50, v41, v46
	v_min_f32_e32 v41, v41, v46
	v_max_f32_e32 v46, v33, v43
	v_min_f32_e32 v43, v33, v43
	v_max_f32_e32 v51, v34, v32
	v_min_f32_e32 v52, v34, v32
	v_max_f32_e32 v32, v35, v47
	v_min_f32_e32 v33, v35, v47
	v_max_f32_e32 v34, v37, v39
	v_min_f32_e32 v35, v37, v39
	v_max_f32_e32 v36, v44, v49
	v_min_f32_e32 v37, v44, v49
	v_max_f32_e32 v38, v42, v40
	v_min_f32_e32 v39, v42, v40
	v_max_f32_e32 v40, v45, v50
	v_min_f32_e32 v42, v45, v50
	v_max_f32_e32 v44, v48, v41
	v_min_f32_e32 v41, v48, v41
	v_max_f32_e32 v45, v46, v51
	v_min_f32_e32 v46, v46, v51
	v_max_f32_e32 v47, v43, v52
	v_min_f32_e32 v43, v43, v52
	v_max_f32_e32 v48, v183, v182
	v_min_f32_e32 v49, v183, v182
	v_min_f32_e32 v50, v242, v241
	v_max_f32_e32 v51, v242, v241
	v_max_f32_e32 v52, v244, v243
	v_min_f32_e32 v53, v244, v243
	v_min_f32_e32 v54, v246, v245
	v_max_f32_e32 v55, v246, v245
	v_max_f32_e32 v56, v248, v247
	v_min_f32_e32 v57, v248, v247
	v_min_f32_e32 v58, v250, v249
	v_max_f32_e32 v59, v250, v249
	v_max_f32_e32 v60, v252, v251
	v_min_f32_e32 v61, v252, v251
	v_min_f32_e32 v62, v195, v190
	v_max_f32_e32 v63, v195, v190
	v_max_f32_e32 v173, v48, v50
	v_min_f32_e32 v48, v48, v50
	v_max_f32_e32 v50, v49, v51
	v_min_f32_e32 v49, v49, v51
	v_min_f32_e32 v51, v52, v54
	v_max_f32_e32 v52, v52, v54
	v_min_f32_e32 v54, v53, v55
	v_max_f32_e32 v53, v53, v55
	v_max_f32_e32 v55, v56, v58
	v_min_f32_e32 v56, v56, v58
	v_max_f32_e32 v58, v57, v59
	v_min_f32_e32 v57, v57, v59
	v_min_f32_e32 v59, v60, v62
	v_max_f32_e32 v60, v60, v62
	v_min_f32_e32 v62, v61, v63
	v_max_f32_e32 v61, v61, v63
	v_max_f32_e32 v63, v173, v50
	v_min_f32_e32 v50, v173, v50
	v_max_f32_e32 v173, v48, v49
	v_min_f32_e32 v48, v48, v49
	v_min_f32_e32 v49, v51, v54
	v_max_f32_e32 v51, v51, v54
	v_min_f32_e32 v54, v52, v53
	v_max_f32_e32 v52, v52, v53
	v_max_f32_e32 v53, v55, v58
	v_min_f32_e32 v55, v55, v58
	v_max_f32_e32 v58, v56, v57
	v_min_f32_e32 v56, v56, v57
	v_min_f32_e32 v57, v59, v62
	v_max_f32_e32 v59, v59, v62
	v_min_f32_e32 v62, v60, v61
	v_max_f32_e32 v60, v60, v61
	v_max_f32_e32 v61, v63, v49
	v_min_f32_e32 v49, v63, v49
	v_max_f32_e32 v63, v50, v51
	v_min_f32_e32 v50, v50, v51
	v_max_f32_e32 v51, v173, v54
	v_min_f32_e32 v54, v173, v54
	v_max_f32_e32 v173, v48, v52
	v_min_f32_e32 v48, v48, v52
	v_min_f32_e32 v52, v53, v57
	v_max_f32_e32 v53, v53, v57
	v_min_f32_e32 v57, v55, v59
	v_max_f32_e32 v55, v55, v59
	v_min_f32_e32 v59, v58, v62
	v_max_f32_e32 v58, v58, v62
	v_min_f32_e32 v62, v56, v60
	v_max_f32_e32 v56, v56, v60
	v_max_f32_e32 v60, v61, v51
	v_min_f32_e32 v51, v61, v51
	v_max_f32_e32 v61, v63, v173
	v_min_f32_e32 v63, v63, v173
	v_max_f32_e32 v173, v49, v54
	v_min_f32_e32 v49, v49, v54
	v_max_f32_e32 v54, v50, v48
	v_min_f32_e32 v48, v50, v48
	v_min_f32_e32 v50, v52, v59
	v_max_f32_e32 v52, v52, v59
	v_min_f32_e32 v59, v57, v62
	v_max_f32_e32 v57, v57, v62
	v_min_f32_e32 v62, v53, v58
	v_max_f32_e32 v53, v53, v58
	v_min_f32_e32 v58, v55, v56
	v_max_f32_e32 v55, v55, v56
	v_max_f32_e32 v56, v60, v61
	v_min_f32_e32 v60, v60, v61
	v_max_f32_e32 v61, v51, v63
	v_min_f32_e32 v51, v51, v63
	v_max_f32_e32 v63, v173, v54
	v_min_f32_e32 v54, v173, v54
	v_max_f32_e32 v173, v49, v48
	v_min_f32_e32 v48, v49, v48
	v_min_f32_e32 v49, v50, v59
	v_max_f32_e32 v50, v50, v59
	v_min_f32_e32 v59, v52, v57
	v_max_f32_e32 v52, v52, v57
	v_min_f32_e32 v57, v62, v58
	v_max_f32_e32 v58, v62, v58
	v_min_f32_e32 v62, v53, v55
	v_max_f32_e32 v53, v53, v55
	v_max_f32_e32 v55, v56, v49
	v_min_f32_e32 v49, v56, v49
	v_max_f32_e32 v56, v60, v50
	v_min_f32_e32 v50, v60, v50
	v_max_f32_e32 v60, v61, v59
	v_min_f32_e32 v59, v61, v59
	v_max_f32_e32 v61, v51, v52
	v_min_f32_e32 v51, v51, v52
	v_max_f32_e32 v52, v63, v57
	v_min_f32_e32 v57, v63, v57
	v_max_f32_e32 v63, v54, v58
	v_min_f32_e32 v54, v54, v58
	v_max_f32_e32 v58, v173, v62
	v_min_f32_e32 v62, v173, v62
	v_max_f32_e32 v173, v48, v53
	v_min_f32_e32 v48, v48, v53
	v_max_f32_e32 v53, v55, v52
	v_min_f32_e32 v52, v55, v52
	v_max_f32_e32 v55, v56, v63
	v_min_f32_e32 v56, v56, v63
	v_max_f32_e32 v63, v60, v58
	v_min_f32_e32 v58, v60, v58
	v_max_f32_e32 v60, v61, v173
	v_min_f32_e32 v61, v61, v173
	v_max_f32_e32 v173, v49, v57
	v_min_f32_e32 v49, v49, v57
	v_max_f32_e32 v57, v50, v54
	v_min_f32_e32 v50, v50, v54
	v_max_f32_e32 v54, v59, v62
	v_min_f32_e32 v59, v59, v62
	v_max_f32_e32 v62, v51, v48
	v_min_f32_e32 v48, v51, v48
	v_max_f32_e32 v51, v53, v63
	v_min_f32_e32 v53, v53, v63
	v_max_f32_e32 v63, v55, v60
	v_min_f32_e32 v55, v55, v60
	v_max_f32_e32 v60, v52, v58
	v_min_f32_e32 v52, v52, v58
	v_max_f32_e32 v58, v56, v61
	v_min_f32_e32 v56, v56, v61
	v_max_f32_e32 v61, v173, v54
	v_min_f32_e32 v54, v173, v54
	v_max_f32_e32 v173, v57, v62
	v_min_f32_e32 v57, v57, v62
	v_max_f32_e32 v62, v49, v59
	v_min_f32_e32 v49, v49, v59
	v_max_f32_e32 v59, v50, v48
	v_min_f32_e32 v48, v50, v48
	v_max_f32_e32 v50, v51, v63
	v_min_f32_e32 v51, v51, v63
	v_max_f32_e32 v63, v53, v55
	v_min_f32_e32 v53, v53, v55
	v_max_f32_e32 v55, v60, v58
	v_min_f32_e32 v58, v60, v58
	v_max_f32_e32 v60, v52, v56
	v_min_f32_e32 v52, v52, v56
	v_max_f32_e32 v56, v61, v173
	v_min_f32_e32 v61, v61, v173
	v_max_f32_e32 v173, v54, v57
	v_min_f32_e32 v54, v54, v57
	v_max_f32_e32 v57, v62, v59
	v_min_f32_e32 v59, v62, v59
	v_max_f32_e32 v62, v49, v48
	v_min_f32_e32 v48, v49, v48
	v_max_f32_e32 v49, v1, v0
	v_min_f32_e32 v0, v1, v0
	v_min_f32_e32 v1, v3, v2
	v_max_f32_e32 v2, v3, v2
	v_max_f32_e32 v3, v5, v4
	v_min_f32_e32 v4, v5, v4
	v_min_f32_e32 v5, v7, v6
	v_max_f32_e32 v6, v7, v6
	v_max_f32_e32 v7, v9, v8
	v_min_f32_e32 v8, v9, v8
	v_min_f32_e32 v9, v11, v10
	v_max_f32_e32 v10, v11, v10
	v_max_f32_e32 v11, v16, v12
	v_min_f32_e32 v12, v16, v12
	v_min_f32_e32 v16, v28, v25
	v_max_f32_e32 v25, v28, v25
	v_max_f32_e32 v28, v49, v1
	v_min_f32_e32 v1, v49, v1
	v_max_f32_e32 v49, v0, v2
	v_min_f32_e32 v0, v0, v2
	v_min_f32_e32 v2, v3, v5
	v_max_f32_e32 v3, v3, v5
	v_min_f32_e32 v5, v4, v6
	v_max_f32_e32 v4, v4, v6
	v_max_f32_e32 v6, v7, v9
	v_min_f32_e32 v7, v7, v9
	v_max_f32_e32 v9, v8, v10
	v_min_f32_e32 v8, v8, v10
	v_min_f32_e32 v10, v11, v16
	v_max_f32_e32 v11, v11, v16
	v_min_f32_e32 v16, v12, v25
	v_max_f32_e32 v12, v12, v25
	v_max_f32_e32 v25, v28, v49
	v_min_f32_e32 v28, v28, v49
	v_max_f32_e32 v49, v1, v0
	v_min_f32_e32 v0, v1, v0
	v_min_f32_e32 v1, v2, v5
	v_max_f32_e32 v2, v2, v5
	v_min_f32_e32 v5, v3, v4
	v_max_f32_e32 v3, v3, v4
	v_max_f32_e32 v4, v6, v9
	v_min_f32_e32 v6, v6, v9
	v_max_f32_e32 v9, v7, v8
	v_min_f32_e32 v7, v7, v8
	v_min_f32_e32 v8, v10, v16
	v_max_f32_e32 v10, v10, v16
	v_min_f32_e32 v16, v11, v12
	v_max_f32_e32 v11, v11, v12
	v_max_f32_e32 v12, v25, v1
	v_min_f32_e32 v1, v25, v1
	v_max_f32_e32 v25, v28, v2
	v_min_f32_e32 v2, v28, v2
	v_max_f32_e32 v28, v49, v5
	v_min_f32_e32 v5, v49, v5
	v_max_f32_e32 v49, v0, v3
	v_min_f32_e32 v0, v0, v3
	v_min_f32_e32 v3, v4, v8
	v_max_f32_e32 v4, v4, v8
	v_min_f32_e32 v8, v6, v10
	v_max_f32_e32 v6, v6, v10
	v_min_f32_e32 v10, v9, v16
	v_max_f32_e32 v9, v9, v16
	v_min_f32_e32 v16, v7, v11
	v_max_f32_e32 v7, v7, v11
	v_max_f32_e32 v11, v12, v28
	v_min_f32_e32 v12, v12, v28
	v_max_f32_e32 v28, v25, v49
	v_min_f32_e32 v25, v25, v49
	v_max_f32_e32 v49, v1, v5
	v_min_f32_e32 v1, v1, v5
	v_max_f32_e32 v5, v2, v0
	v_min_f32_e32 v0, v2, v0
	v_min_f32_e32 v2, v3, v10
	v_max_f32_e32 v3, v3, v10
	v_min_f32_e32 v10, v8, v16
	v_max_f32_e32 v8, v8, v16
	v_min_f32_e32 v16, v4, v9
	v_max_f32_e32 v4, v4, v9
	v_min_f32_e32 v9, v6, v7
	v_max_f32_e32 v6, v6, v7
	v_max_f32_e32 v7, v11, v28
	v_min_f32_e32 v11, v11, v28
	v_max_f32_e32 v28, v12, v25
	v_min_f32_e32 v12, v12, v25
	v_max_f32_e32 v25, v49, v5
	v_min_f32_e32 v5, v49, v5
	v_max_f32_e32 v49, v1, v0
	v_min_f32_e32 v0, v1, v0
	v_min_f32_e32 v1, v2, v10
	v_max_f32_e32 v2, v2, v10
	v_min_f32_e32 v10, v3, v8
	v_max_f32_e32 v3, v3, v8
	v_min_f32_e32 v8, v16, v9
	v_max_f32_e32 v9, v16, v9
	v_min_f32_e32 v16, v4, v6
	v_max_f32_e32 v4, v4, v6
	v_max_f32_e32 v6, v7, v1
	v_min_f32_e32 v1, v7, v1
	v_max_f32_e32 v7, v11, v2
	v_min_f32_e32 v2, v11, v2
	v_max_f32_e32 v11, v28, v10
	v_min_f32_e32 v10, v28, v10
	v_max_f32_e32 v28, v12, v3
	v_min_f32_e32 v3, v12, v3
	v_max_f32_e32 v12, v25, v8
	v_min_f32_e32 v8, v25, v8
	v_max_f32_e32 v25, v5, v9
	v_min_f32_e32 v5, v5, v9
	v_max_f32_e32 v9, v49, v16
	v_min_f32_e32 v16, v49, v16
	v_max_f32_e32 v49, v0, v4
	v_min_f32_e32 v0, v0, v4
	v_max_f32_e32 v4, v6, v12
	v_min_f32_e32 v6, v6, v12
	v_max_f32_e32 v12, v7, v25
	v_min_f32_e32 v7, v7, v25
	v_max_f32_e32 v25, v11, v9
	v_min_f32_e32 v9, v11, v9
	v_max_f32_e32 v11, v28, v49
	v_min_f32_e32 v28, v28, v49
	v_max_f32_e32 v49, v1, v8
	v_min_f32_e32 v1, v1, v8
	v_max_f32_e32 v8, v2, v5
	v_min_f32_e32 v2, v2, v5
	v_max_f32_e32 v5, v10, v16
	v_min_f32_e32 v10, v10, v16
	v_max_f32_e32 v16, v3, v0
	v_min_f32_e32 v0, v3, v0
	v_max_f32_e32 v3, v4, v25
	v_min_f32_e32 v4, v4, v25
	v_max_f32_e32 v25, v12, v11
	v_min_f32_e32 v11, v12, v11
	v_max_f32_e32 v12, v6, v9
	v_min_f32_e32 v6, v6, v9
	v_max_f32_e32 v9, v7, v28
	v_min_f32_e32 v7, v7, v28
	v_max_f32_e32 v28, v49, v5
	v_min_f32_e32 v5, v49, v5
	v_max_f32_e32 v49, v8, v16
	v_min_f32_e32 v8, v8, v16
	v_max_f32_e32 v16, v1, v10
	v_min_f32_e32 v1, v1, v10
	v_max_f32_e32 v10, v2, v0
	v_min_f32_e32 v0, v2, v0
	v_max_f32_e32 v2, v3, v25
	v_min_f32_e32 v3, v3, v25
	v_max_f32_e32 v25, v4, v11
	v_min_f32_e32 v4, v4, v11
	v_max_f32_e32 v11, v12, v9
	v_min_f32_e32 v9, v12, v9
	v_max_f32_e32 v12, v6, v7
	v_min_f32_e32 v6, v6, v7
	v_max_f32_e32 v7, v28, v49
	v_min_f32_e32 v28, v28, v49
	v_max_f32_e32 v49, v5, v8
	v_min_f32_e32 v5, v5, v8
	v_max_f32_e32 v8, v16, v10
	v_min_f32_e32 v10, v16, v10
	v_max_f32_e32 v16, v1, v0
	v_min_f32_e32 v0, v1, v0
	v_max_f32_e32 v1, v31, v43
	v_max_f32_e32 v29, v29, v47
	v_max_f32_e32 v30, v30, v46
	v_max_f32_e32 v26, v26, v45
	v_max_f32_e32 v27, v27, v41
	v_max_f32_e32 v23, v23, v44
	v_max_f32_e32 v24, v24, v42
	v_max_f32_e32 v21, v21, v40
	v_max_f32_e32 v22, v22, v39
	v_max_f32_e32 v19, v19, v38
	v_max_f32_e32 v20, v20, v37
	v_max_f32_e32 v17, v17, v36
	v_max_f32_e32 v18, v18, v35
	v_max_f32_e32 v14, v14, v34
	v_max_f32_e32 v15, v15, v33
	v_max_f32_e32 v13, v13, v32
	v_max_f32_e32 v31, v1, v22
	v_min_f32_e32 v1, v1, v22
	v_max_f32_e32 v22, v29, v19
	v_min_f32_e32 v19, v29, v19
	v_max_f32_e32 v29, v30, v20
	v_min_f32_e32 v20, v30, v20
	v_max_f32_e32 v30, v26, v17
	v_min_f32_e32 v17, v26, v17
	v_max_f32_e32 v26, v27, v18
	v_min_f32_e32 v18, v27, v18
	v_max_f32_e32 v27, v23, v14
	v_min_f32_e32 v14, v23, v14
	v_max_f32_e32 v23, v24, v15
	v_min_f32_e32 v15, v24, v15
	v_max_f32_e32 v24, v21, v13
	v_min_f32_e32 v13, v21, v13
	v_max_f32_e32 v21, v31, v26
	v_min_f32_e32 v26, v31, v26
	v_max_f32_e32 v31, v22, v27
	v_min_f32_e32 v22, v22, v27
	v_max_f32_e32 v27, v29, v23
	v_min_f32_e32 v23, v29, v23
	v_max_f32_e32 v29, v30, v24
	v_min_f32_e32 v24, v30, v24
	v_max_f32_e32 v30, v1, v18
	v_min_f32_e32 v1, v1, v18
	v_max_f32_e32 v18, v19, v14
	v_min_f32_e32 v14, v19, v14
	v_max_f32_e32 v19, v20, v15
	v_min_f32_e32 v15, v20, v15
	v_max_f32_e32 v20, v17, v13
	v_min_f32_e32 v13, v17, v13
	v_max_f32_e32 v17, v21, v27
	v_min_f32_e32 v21, v21, v27
	v_max_f32_e32 v27, v31, v29
	v_min_f32_e32 v29, v31, v29
	v_max_f32_e32 v31, v26, v23
	v_min_f32_e32 v23, v26, v23
	v_max_f32_e32 v26, v22, v24
	v_min_f32_e32 v22, v22, v24
	v_max_f32_e32 v24, v30, v19
	v_min_f32_e32 v19, v30, v19
	v_max_f32_e32 v30, v18, v20
	v_min_f32_e32 v18, v18, v20
	v_max_f32_e32 v20, v1, v15
	v_min_f32_e32 v1, v1, v15
	v_max_f32_e32 v15, v14, v13
	v_min_f32_e32 v13, v14, v13
	v_max_f32_e32 v14, v17, v27
	v_min_f32_e32 v17, v17, v27
	v_max_f32_e32 v27, v21, v29
	v_min_f32_e32 v21, v21, v29
	v_max_f32_e32 v29, v31, v26
	v_min_f32_e32 v26, v31, v26
	v_max_f32_e32 v31, v23, v22
	v_min_f32_e32 v22, v23, v22
	v_max_f32_e32 v23, v24, v30
	v_min_f32_e32 v24, v24, v30
	v_max_f32_e32 v30, v19, v18
	v_min_f32_e32 v18, v19, v18
	v_max_f32_e32 v19, v20, v15
	v_min_f32_e32 v15, v20, v15
	v_max_f32_e32 v20, v1, v13
	v_min_f32_e32 v1, v1, v13
	v_max_f32_e32 v0, v50, v0
	v_max_f32_e32 v13, v51, v16
	v_max_f32_e32 v10, v63, v10
	v_max_f32_e32 v8, v53, v8
	v_max_f32_e32 v5, v55, v5
	v_max_f32_e32 v16, v58, v49
	v_max_f32_e32 v28, v60, v28
	v_max_f32_e32 v7, v52, v7
	v_max_f32_e32 v6, v56, v6
	v_max_f32_e32 v12, v61, v12
	v_max_f32_e32 v9, v173, v9
	v_max_f32_e32 v11, v54, v11
	v_max_f32_e32 v4, v57, v4
	v_max_f32_e32 v25, v59, v25
	v_max_f32_e32 v3, v62, v3
	v_max_f32_e32 v2, v48, v2
	v_max_f32_e32 v32, v0, v6
	v_min_f32_e32 v0, v0, v6
	v_max_f32_e32 v6, v13, v12
	v_min_f32_e32 v12, v13, v12
	v_max_f32_e32 v13, v10, v9
	v_min_f32_e32 v9, v10, v9
	v_max_f32_e32 v10, v8, v11
	v_min_f32_e32 v8, v8, v11
	v_max_f32_e32 v11, v5, v4
	v_min_f32_e32 v4, v5, v4
	v_max_f32_e32 v5, v16, v25
	v_min_f32_e32 v16, v16, v25
	v_max_f32_e32 v25, v28, v3
	v_min_f32_e32 v3, v28, v3
	v_max_f32_e32 v28, v7, v2
	v_min_f32_e32 v2, v7, v2
	v_max_f32_e32 v7, v32, v11
	v_min_f32_e32 v11, v32, v11
	v_max_f32_e32 v32, v6, v5
	v_min_f32_e32 v5, v6, v5
	v_max_f32_e32 v6, v13, v25
	v_min_f32_e32 v13, v13, v25
	v_max_f32_e32 v25, v10, v28
	v_min_f32_e32 v10, v10, v28
	v_max_f32_e32 v28, v0, v4
	v_min_f32_e32 v0, v0, v4
	v_max_f32_e32 v4, v12, v16
	v_min_f32_e32 v12, v12, v16
	v_max_f32_e32 v16, v9, v3
	v_min_f32_e32 v3, v9, v3
	v_max_f32_e32 v9, v8, v2
	v_min_f32_e32 v2, v8, v2
	v_max_f32_e32 v8, v7, v6
	v_min_f32_e32 v6, v7, v6
	v_max_f32_e32 v7, v32, v25
	v_min_f32_e32 v25, v32, v25
	v_max_f32_e32 v32, v11, v13
	v_min_f32_e32 v11, v11, v13
	v_max_f32_e32 v13, v5, v10
	v_min_f32_e32 v5, v5, v10
	v_max_f32_e32 v10, v28, v16
	v_min_f32_e32 v16, v28, v16
	v_max_f32_e32 v28, v4, v9
	v_min_f32_e32 v4, v4, v9
	v_max_f32_e32 v9, v0, v3
	v_min_f32_e32 v0, v0, v3
	v_max_f32_e32 v3, v12, v2
	v_min_f32_e32 v2, v12, v2
	v_max_f32_e32 v12, v8, v7
	v_min_f32_e32 v7, v8, v7
	v_max_f32_e32 v8, v6, v25
	v_min_f32_e32 v6, v6, v25
	v_max_f32_e32 v25, v32, v13
	v_min_f32_e32 v13, v32, v13
	v_max_f32_e32 v32, v11, v5
	v_min_f32_e32 v5, v11, v5
	v_max_f32_e32 v11, v10, v28
	v_min_f32_e32 v10, v10, v28
	v_max_f32_e32 v28, v16, v4
	v_min_f32_e32 v4, v16, v4
	v_max_f32_e32 v16, v9, v3
	v_min_f32_e32 v3, v9, v3
	v_max_f32_e32 v9, v0, v2
	v_min_f32_e32 v0, v0, v2
	v_max_f32_e32 v0, v14, v0
	v_max_f32_e32 v2, v17, v9
	v_max_f32_e32 v3, v27, v3
	v_max_f32_e32 v9, v21, v16
	v_max_f32_e32 v4, v29, v4
	v_max_f32_e32 v14, v26, v28
	v_max_f32_e32 v10, v31, v10
	v_max_f32_e32 v11, v22, v11
	v_max_f32_e32 v5, v23, v5
	v_max_f32_e32 v16, v24, v32
	v_max_f32_e32 v13, v30, v13
	v_max_f32_e32 v17, v18, v25
	v_max_f32_e32 v6, v19, v6
	v_max_f32_e32 v8, v15, v8
	v_max_f32_e32 v7, v20, v7
	v_max_f32_e32 v1, v1, v12
	v_max_f32_e32 v12, v0, v5
	v_min_f32_e32 v0, v0, v5
	v_max_f32_e32 v5, v2, v16
	v_min_f32_e32 v2, v2, v16
	v_max_f32_e32 v15, v3, v13
	v_min_f32_e32 v3, v3, v13
	v_max_f32_e32 v13, v9, v17
	v_min_f32_e32 v9, v9, v17
	v_max_f32_e32 v16, v4, v6
	v_min_f32_e32 v4, v4, v6
	v_max_f32_e32 v6, v14, v8
	v_min_f32_e32 v8, v14, v8
	v_max_f32_e32 v14, v10, v7
	v_min_f32_e32 v7, v10, v7
	v_max_f32_e32 v10, v11, v1
	v_min_f32_e32 v1, v11, v1
	v_max_f32_e32 v11, v12, v16
	v_min_f32_e32 v12, v12, v16
	v_max_f32_e32 v16, v5, v6
	v_min_f32_e32 v5, v5, v6
	v_max_f32_e32 v6, v15, v14
	v_min_f32_e32 v14, v15, v14
	v_max_f32_e32 v15, v13, v10
	v_min_f32_e32 v10, v13, v10
	v_max_f32_e32 v13, v0, v4
	v_min_f32_e32 v0, v0, v4
	v_max_f32_e32 v4, v2, v8
	v_min_f32_e32 v2, v2, v8
	v_max_f32_e32 v8, v3, v7
	v_min_f32_e32 v3, v3, v7
	v_max_f32_e32 v7, v9, v1
	v_min_f32_e32 v1, v9, v1
	v_max_f32_e32 v9, v11, v6
	v_min_f32_e32 v6, v11, v6
	v_max_f32_e32 v11, v16, v15
	v_min_f32_e32 v15, v16, v15
	v_max_f32_e32 v16, v12, v14
	v_min_f32_e32 v12, v12, v14
	v_max_f32_e32 v14, v5, v10
	v_min_f32_e32 v5, v5, v10
	v_max_f32_e32 v10, v13, v8
	v_min_f32_e32 v8, v13, v8
	v_max_f32_e32 v13, v4, v7
	v_min_f32_e32 v4, v4, v7
	v_max_f32_e32 v7, v0, v3
	v_min_f32_e32 v0, v0, v3
	v_max_f32_e32 v3, v2, v1
	v_min_f32_e32 v1, v2, v1
	v_max_f32_e32 v2, v9, v11
	v_min_f32_e32 v9, v9, v11
	v_max_f32_e32 v11, v6, v15
	v_min_f32_e32 v6, v6, v15
	v_max_f32_e32 v15, v16, v14
	v_min_f32_e32 v14, v16, v14
	v_max_f32_e32 v16, v12, v5
	v_min_f32_e32 v5, v12, v5
	v_max_f32_e32 v12, v10, v13
	v_min_f32_e32 v10, v10, v13
	v_max_f32_e32 v13, v8, v4
	v_min_f32_e32 v4, v8, v4
	v_max_f32_e32 v8, v7, v3
	v_min_f32_e32 v3, v7, v3
	v_max_f32_e32 v7, v0, v1
	v_min_f32_e32 v0, v0, v1
	v_mov_b32_e32 v27, v0
	s_nop 1
	v_permlane32_swap_b32 v27, v27
	v_mov_b32_e32 v29, v7
	s_nop 1
	v_permlane32_swap_b32 v29, v29
	v_mov_b32_e32 v31, v3
	s_nop 1
	v_permlane32_swap_b32 v31, v31
	v_mov_b32_e32 v30, v8
	s_nop 1
	v_permlane32_swap_b32 v30, v30
	v_mov_b32_e32 v28, v4
	s_nop 1
	v_permlane32_swap_b32 v28, v28
	v_mov_b32_e32 v26, v13
	s_nop 1
	v_permlane32_swap_b32 v26, v26
	s_waitcnt lgkmcnt(5)
	v_mov_b32_e32 v1, v2
	s_nop 1
	v_permlane32_swap_b32 v1, v1
	v_mov_b32_e32 v25, v10
	s_nop 1
	v_permlane32_swap_b32 v25, v25
	v_max_f32_e32 v2, v2, v27
	s_waitcnt lgkmcnt(6)
	v_mov_b32_e32 v17, v9
	s_nop 1
	v_permlane32_swap_b32 v17, v17
	v_mov_b32_e32 v24, v12
	s_nop 1
	v_permlane32_swap_b32 v24, v24
	v_max_f32_e32 v9, v9, v29
	s_waitcnt lgkmcnt(7)
	v_mov_b32_e32 v18, v11
	s_nop 1
	v_permlane32_swap_b32 v18, v18
	v_mov_b32_e32 v23, v5
	s_nop 1
	v_permlane32_swap_b32 v23, v23
	v_max_f32_e32 v11, v11, v31
	s_waitcnt lgkmcnt(8)
	v_mov_b32_e32 v19, v6
	s_nop 1
	v_permlane32_swap_b32 v19, v19
	v_mov_b32_e32 v22, v16
	s_nop 1
	v_permlane32_swap_b32 v22, v22
	v_max_f32_e32 v6, v6, v30
	s_waitcnt lgkmcnt(9)
	v_mov_b32_e32 v20, v15
	s_nop 1
	v_permlane32_swap_b32 v20, v20
	v_mov_b32_e32 v21, v14
	s_nop 1
	v_permlane32_swap_b32 v21, v21
	v_max_f32_e32 v15, v15, v28
	s_waitcnt lgkmcnt(10)
	v_max_f32_e32 v14, v14, v26
	s_waitcnt lgkmcnt(8)
	v_max_f32_e32 v16, v16, v25
	s_waitcnt lgkmcnt(6)
	v_max_f32_e32 v5, v5, v24
	s_waitcnt lgkmcnt(4)
	v_max_f32_e32 v12, v12, v23
	s_waitcnt lgkmcnt(2)
	v_max_f32_e32 v10, v10, v22
	s_waitcnt lgkmcnt(0)
	v_max_f32_e32 v13, v13, v21
	v_max_f32_e32 v4, v4, v20
	v_max_f32_e32 v8, v8, v19
	v_max_f32_e32 v3, v3, v18
	v_max_f32_e32 v7, v7, v17
	v_max_f32_e32 v0, v0, v1
	v_max_f32_e32 v1, v2, v12
	v_min_f32_e32 v2, v2, v12
	v_max_f32_e32 v12, v9, v10
	v_min_f32_e32 v9, v9, v10
	v_max_f32_e32 v10, v11, v13
	v_min_f32_e32 v11, v11, v13
	v_max_f32_e32 v13, v6, v4
	v_min_f32_e32 v4, v6, v4
	v_max_f32_e32 v6, v15, v8
	v_min_f32_e32 v8, v15, v8
	v_max_f32_e32 v15, v14, v3
	v_min_f32_e32 v3, v14, v3
	v_max_f32_e32 v14, v16, v7
	v_min_f32_e32 v7, v16, v7
	v_max_f32_e32 v16, v5, v0
	v_min_f32_e32 v0, v5, v0
	v_max_f32_e32 v5, v1, v6
	v_min_f32_e32 v1, v1, v6
	v_max_f32_e32 v6, v12, v15
	v_min_f32_e32 v12, v12, v15
	v_max_f32_e32 v15, v10, v14
	v_min_f32_e32 v10, v10, v14
	v_max_f32_e32 v14, v13, v16
	v_min_f32_e32 v13, v13, v16
	v_max_f32_e32 v16, v2, v8
	v_min_f32_e32 v2, v2, v8
	v_max_f32_e32 v8, v9, v3
	v_min_f32_e32 v3, v9, v3
	v_max_f32_e32 v9, v11, v7
	v_min_f32_e32 v7, v11, v7
	v_max_f32_e32 v11, v4, v0
	v_min_f32_e32 v0, v4, v0
	v_max_f32_e32 v4, v5, v15
	v_min_f32_e32 v5, v5, v15
	v_max_f32_e32 v15, v6, v14
	v_min_f32_e32 v6, v6, v14
	v_max_f32_e32 v14, v1, v10
	v_min_f32_e32 v1, v1, v10
	v_max_f32_e32 v10, v12, v13
	v_min_f32_e32 v12, v12, v13
	v_max_f32_e32 v13, v16, v9
	v_min_f32_e32 v9, v16, v9
	v_max_f32_e32 v16, v8, v11
	v_min_f32_e32 v8, v8, v11
	v_max_f32_e32 v11, v2, v7
	v_min_f32_e32 v2, v2, v7
	v_max_f32_e32 v7, v3, v0
	v_min_f32_e32 v0, v3, v0
	v_max_f32_e32 v3, v4, v15
	v_min_f32_e32 v4, v4, v15
	v_max_f32_e32 v15, v5, v6
	v_min_f32_e32 v5, v5, v6
	v_max_f32_e32 v6, v14, v10
	v_min_f32_e32 v10, v14, v10
	v_max_f32_e32 v14, v1, v12
	v_min_f32_e32 v1, v1, v12
	v_max_f32_e32 v12, v13, v16
	v_min_f32_e32 v13, v13, v16
	v_max_f32_e32 v16, v9, v8
	v_min_f32_e32 v8, v9, v8
	v_max_f32_e32 v9, v11, v7
	v_min_f32_e32 v7, v11, v7
	v_max_f32_e32 v11, v2, v0
	v_min_f32_e32 v0, v2, v0
	v_lshl_add_u32 v2, s8, 12, v207
	ds_write2st64_b32 v2, v3, v4 offset1:1
	ds_write2st64_b32 v2, v15, v5 offset0:2 offset1:3
	ds_write2st64_b32 v2, v6, v10 offset0:4 offset1:5
	ds_write2st64_b32 v2, v14, v1 offset0:6 offset1:7
	ds_write2st64_b32 v2, v12, v13 offset0:8 offset1:9
	ds_write2st64_b32 v2, v16, v8 offset0:10 offset1:11
	ds_write2st64_b32 v2, v9, v7 offset0:12 offset1:13
	ds_write2st64_b32 v2, v11, v0 offset0:14 offset1:15
	s_mov_b64 s[6:7], 0
	s_mov_b32 s8, 1
	s_cbranch_vccz .LBB0_704
	ds_read2st64_b32 v[0:1], v207 offset1:1
	ds_read2st64_b32 v[2:3], v207 offset0:2 offset1:3
	ds_read2st64_b32 v[4:5], v207 offset0:4 offset1:5
	ds_read2st64_b32 v[6:7], v207 offset0:6 offset1:7
	ds_read2st64_b32 v[16:17], v207 offset0:16 offset1:17
	ds_read2st64_b32 v[18:19], v207 offset0:18 offset1:19
	ds_read2st64_b32 v[20:21], v207 offset0:20 offset1:21
	ds_read2st64_b32 v[22:23], v207 offset0:22 offset1:23
	ds_read2st64_b32 v[8:9], v207 offset0:8 offset1:9
	ds_read2st64_b32 v[10:11], v207 offset0:10 offset1:11
	ds_read2st64_b32 v[12:13], v207 offset0:12 offset1:13
	ds_read2st64_b32 v[14:15], v207 offset0:14 offset1:15
	ds_read2st64_b32 v[24:25], v207 offset0:24 offset1:25
	ds_read2st64_b32 v[26:27], v207 offset0:26 offset1:27
	ds_read2st64_b32 v[28:29], v207 offset0:28 offset1:29
	ds_read2st64_b32 v[30:31], v207 offset0:30 offset1:31
	s_and_saveexec_b64 s[8:9], s[38:39]
	s_cbranch_execz .LBB0_696
	s_waitcnt lgkmcnt(0)
	v_and_b32_e32 v49, 0xffffff80, v30
	v_and_b32_e32 v48, 0xffffff80, v0
	v_and_b32_e32 v39, 0xffffff80, v19
	v_and_b32_e32 v38, 0xffffff80, v20
	v_pk_add_f32 v[52:53], v[38:39], v[48:49] op_sel:[1,0] op_sel_hi:[0,1]
	v_cmp_gt_i32_e32 vcc, 0, v52
	v_bfrev_b32_e32 v43, 0.5
	s_movk_i32 s12, 0xff00
	v_cndmask_b32_e64 v43, v43, 3, vcc
	v_and_b32_e32 v42, 0xffffff80, v23
	v_and_or_b32 v56, v52, s12, v43
	v_mov_b32_e32 v43, v38
	v_pk_add_f32 v[52:53], v[48:49], v[42:43] op_sel_hi:[0,1]
	v_cmp_gt_i32_e32 vcc, 0, v53
	v_mov_b32_e32 v54, 0xfb
	v_and_b32_e32 v41, 0xffffff80, v22
	v_cndmask_b32_e64 v54, v54, 4, vcc
	v_and_b32_e32 v40, 0xffffff80, v21
	v_and_or_b32 v53, v53, s12, v54
	v_cmp_gt_i32_e32 vcc, 0, v52
	v_mov_b32_e32 v54, 0xf8
	v_mov_b32_e32 v58, 0xf9
	v_cndmask_b32_e64 v57, v54, 7, vcc
	v_pk_add_f32 v[54:55], v[48:49], v[40:41] op_sel_hi:[0,1]
	v_cmp_gt_i32_e32 vcc, 0, v55
	v_mov_b32_e32 v59, 0xfa
	v_and_b32_e32 v55, 0xffffff00, v55
	v_cndmask_b32_e64 v58, v58, 6, vcc
	v_cmp_gt_i32_e32 vcc, 0, v54
	v_and_b32_e32 v54, 0xffffff00, v54
	v_and_b32_e32 v52, 0xffffff00, v52
	v_cndmask_b32_e64 v59, v59, 5, vcc
	v_or_b32_e32 v55, v58, v55
	v_or_b32_e32 v54, v59, v54
	v_or_b32_e32 v52, v57, v52
	v_writelane_b32 v255, s8, 44
	v_min_f32_e32 v57, v55, v52
	v_max_f32_e32 v58, v53, v54
	v_min_f32_e32 v53, v53, v54
	v_max_f32_e32 v52, v55, v52
	v_writelane_b32 v255, s9, 45
	v_and_b32_e32 v45, 0xffffff80, v24
	v_and_b32_e32 v44, 0xffffff80, v27
	v_min_f32_e32 v59, v58, v57
	v_min_f32_e32 v54, v53, v52
	v_max_f32_e32 v57, v58, v57
	v_max_f32_e32 v52, v53, v52
	v_pk_add_f32 v[44:45], v[48:49], v[44:45] op_sel_hi:[0,1]
	v_and_b32_e32 v47, 0xffffff80, v26
	v_min_f32_e32 v58, v57, v52
	v_max_f32_e32 v57, v57, v52
	v_cmp_gt_i32_e32 vcc, 0, v45
	v_mov_b32_e32 v52, 0xf7
	v_and_b32_e32 v46, 0xffffff80, v25
	v_cndmask_b32_e64 v52, v52, 8, vcc
	v_and_or_b32 v45, v45, s12, v52
	v_cmp_gt_i32_e32 vcc, 0, v44
	v_mov_b32_e32 v52, 0xf4
	v_pk_add_f32 v[46:47], v[48:49], v[46:47] op_sel_hi:[0,1]
	v_cndmask_b32_e64 v52, v52, 11, vcc
	v_cmp_gt_i32_e32 vcc, 0, v47
	v_mov_b32_e32 v53, 0xf5
	v_min_f32_e32 v55, v59, v54
	v_max_f32_e32 v59, v59, v54
	v_cndmask_b32_e64 v53, v53, 10, vcc
	v_cmp_gt_i32_e32 vcc, 0, v46
	v_mov_b32_e32 v54, 0xf6
	v_and_b32_e32 v47, 0xffffff00, v47
	v_cndmask_b32_e64 v54, v54, 9, vcc
	v_and_b32_e32 v46, 0xffffff00, v46
	v_and_b32_e32 v44, 0xffffff00, v44
	v_or_b32_e32 v47, v53, v47
	v_or_b32_e32 v46, v54, v46
	v_or_b32_e32 v44, v52, v44
	v_and_b32_e32 v51, 0xffffff80, v29
	v_and_b32_e32 v50, 0xffffff80, v28
	v_writelane_b32 v255, s11, 46
	v_min_f32_e32 v52, v47, v44
	v_max_f32_e32 v53, v45, v46
	v_min_f32_e32 v46, v45, v46
	v_max_f32_e32 v47, v47, v44
	v_pk_add_f32 v[44:45], v[48:49], v[50:51] op_sel_hi:[0,1]
	v_cmp_gt_i32_e64 s[10:11], 0, v45
	v_mov_b32_e32 v50, 0xf2
	v_mov_b32_e32 v51, 0xf3
	v_cndmask_b32_e64 v50, v50, 13, s[10:11]
	v_cmp_gt_i32_e64 s[10:11], 0, v44
	v_and_b32_e32 v45, 0xffffff00, v45
	v_and_b32_e32 v44, 0xffffff00, v44
	v_cndmask_b32_e64 v51, v51, 12, s[10:11]
	v_or_b32_e32 v50, v50, v45
	v_or_b32_e32 v51, v51, v44
	v_and_b32_e32 v45, 0xffffff80, v31
	v_mov_b32_e32 v44, v49
	v_pk_add_f32 v[44:45], v[48:49], v[44:45] op_sel_hi:[0,1]
	v_cmp_gt_i32_e64 s[42:43], 0, v45
	v_mov_b32_e32 v249, 0xf0
	v_mov_b32_e32 v173, 0xf1
	v_cndmask_b32_e64 v63, v249, 15, s[42:43]
	v_cmp_gt_i32_e64 s[42:43], 0, v44
	v_and_b32_e32 v45, 0xffffff00, v45
	v_and_b32_e32 v44, 0xffffff00, v44
	v_cndmask_b32_e64 v173, v173, 14, s[42:43]
	v_or_b32_e32 v45, v63, v45
	v_or_b32_e32 v44, v173, v44
	v_max_f32_e32 v62, v51, v50
	v_min_f32_e32 v63, v44, v45
	v_min_f32_e32 v50, v51, v50
	v_max_f32_e32 v44, v44, v45
	v_max_f32_e32 v54, v53, v52
	v_max_f32_e32 v60, v46, v47
	v_min_f32_e32 v173, v62, v63
	v_min_f32_e32 v45, v50, v44
	v_min_f32_e32 v51, v53, v52
	v_min_f32_e32 v46, v46, v47
	v_max_f32_e32 v52, v62, v63
	v_max_f32_e32 v44, v50, v44
	v_max_f32_e32 v61, v54, v60
	v_min_f32_e32 v178, v173, v45
	v_max_f32_e32 v47, v51, v46
	v_min_f32_e32 v50, v52, v44
	v_min_f32_e32 v54, v54, v60
	v_max_f32_e32 v45, v173, v45
	v_min_f32_e32 v46, v51, v46
	v_max_f32_e32 v44, v52, v44
	v_min_f32_e32 v179, v61, v178
	v_min_f32_e32 v53, v47, v50
	v_min_f32_e32 v60, v54, v45
	v_min_f32_e32 v52, v46, v44
	v_max_f32_e32 v61, v61, v178
	v_max_f32_e32 v47, v47, v50
	v_max_f32_e32 v45, v54, v45
	v_max_f32_e32 v44, v46, v44
	v_min_f32_e32 v62, v179, v53
	v_min_f32_e32 v63, v60, v52
	v_min_f32_e32 v50, v61, v47
	v_min_f32_e32 v46, v45, v44
	v_max_f32_e32 v53, v179, v53
	v_max_f32_e32 v52, v60, v52
	v_max_f32_e32 v47, v61, v47
	v_max_f32_e32 v44, v45, v44
	v_min_f32_e32 v60, v53, v52
	v_min_f32_e32 v61, v47, v44
	v_max_f32_e32 v52, v53, v52
	v_max_f32_e32 v53, v47, v44
	v_and_b32_e32 v44, 0xffffff80, v1
	v_add_f32_e32 v45, v39, v44
	v_min_f32_e32 v51, v62, v63
	v_min_f32_e32 v173, v50, v46
	v_max_f32_e32 v62, v62, v63
	v_max_f32_e32 v63, v50, v46
	v_cmp_gt_i32_e32 vcc, 0, v45
	v_mov_b32_e32 v46, 0xec
	v_mov_b32_e32 v47, 0xe9
	v_cndmask_b32_e64 v46, v46, 19, vcc
	v_and_or_b32 v45, v45, s12, v46
	v_pk_add_f32 v[42:43], v[44:45], v[42:43] op_sel_hi:[0,1]
	v_cmp_gt_i32_e32 vcc, 0, v43
	v_mov_b32_e32 v46, 0xeb
	v_pk_add_f32 v[40:41], v[44:45], v[40:41] op_sel_hi:[0,1]
	v_cndmask_b32_e64 v46, v46, 20, vcc
	v_and_or_b32 v43, v43, s12, v46
	v_cmp_gt_i32_e32 vcc, 0, v42
	v_mov_b32_e32 v46, 0xe8
	v_mov_b32_e32 v50, 0xea
	v_cndmask_b32_e64 v46, v46, 23, vcc
	v_cmp_gt_i32_e32 vcc, 0, v41
	v_and_b32_e32 v41, 0xffffff00, v41
	v_and_b32_e32 v42, 0xffffff00, v42
	v_cndmask_b32_e64 v47, v47, 22, vcc
	v_cmp_gt_i32_e32 vcc, 0, v40
	v_and_b32_e32 v40, 0xffffff00, v40
	v_or_b32_e32 v41, v47, v41
	v_cndmask_b32_e64 v50, v50, 21, vcc
	v_or_b32_e32 v40, v50, v40
	v_or_b32_e32 v42, v46, v42
	v_and_b32_e32 v182, 0xffffff80, v3
	v_min_f32_e32 v46, v41, v42
	v_max_f32_e32 v47, v43, v40
	v_min_f32_e32 v40, v43, v40
	v_max_f32_e32 v41, v41, v42
	v_and_b32_e32 v37, 0xffffff80, v4
	v_max_f32_e32 v43, v47, v46
	v_min_f32_e32 v42, v40, v41
	v_max_f32_e32 v40, v40, v41
	v_min_f32_e32 v50, v47, v46
	v_and_b32_e32 v46, 0xffffff80, v2
	v_and_b32_e32 v36, 0xffffff80, v18
	v_min_f32_e32 v179, v43, v40
	v_max_f32_e32 v180, v43, v40
	v_pk_add_f32 v[40:41], v[46:47], v[38:39] op_sel_hi:[0,1]
	v_cmp_gt_i32_e32 vcc, 0, v41
	v_mov_b32_e32 v38, 0xdc
	v_and_b32_e32 v35, 0xffffff80, v7
	v_cndmask_b32_e64 v38, v38, 35, vcc
	v_and_or_b32 v41, v41, s12, v38
	v_cmp_gt_i32_e32 vcc, 0, v40
	v_mov_b32_e32 v38, 0xdb
	v_and_b32_e32 v34, 0xffffff80, v17
	v_cndmask_b32_e64 v38, v38, 36, vcc
	v_and_or_b32 v181, v40, s12, v38
	v_add_f32_e32 v38, v39, v182
	v_cmp_gt_i32_e32 vcc, 0, v38
	v_mov_b32_e32 v39, 0xcc
	s_nop 0
	v_cndmask_b32_e64 v39, v39, 51, vcc
	v_and_or_b32 v54, v38, s12, v39
	v_pk_add_f32 v[38:39], v[48:49], v[36:37]
	v_min_f32_e32 v178, v50, v42
	v_cmp_gt_i32_e32 vcc, 0, v38
	v_bfrev_b32_e32 v39, -0.5
	v_max_f32_e32 v50, v50, v42
	v_cndmask_b32_e64 v39, v39, 2, vcc
	v_and_or_b32 v38, v38, s12, v39
	v_mov_b32_e32 v39, 0xed
	v_and_b32_e32 v43, 0xffffff80, v6
	v_min_f32_e32 v183, v38, v56
	v_max_f32_e32 v56, v38, v56
	v_add_f32_e32 v38, v36, v44
	v_cmp_gt_i32_e32 vcc, 0, v38
	v_and_b32_e32 v42, 0xffffff80, v5
	v_and_b32_e32 v33, 0xffffff80, v14
	v_cndmask_b32_e64 v39, v39, 18, vcc
	v_and_or_b32 v38, v38, s12, v39
	v_mov_b32_e32 v39, 0xdd
	v_and_b32_e32 v32, 0xffffff80, v16
	v_min_f32_e32 v190, v38, v45
	v_max_f32_e32 v195, v38, v45
	v_add_f32_e32 v38, v36, v46
	v_cmp_gt_i32_e32 vcc, 0, v38
	v_mov_b32_e32 v45, 0x61
	v_mov_b32_e32 v234, 0xef
	v_cndmask_b32_e64 v39, v39, 34, vcc
	v_and_or_b32 v38, v38, s12, v39
	v_mov_b32_e32 v39, 0xcd
	v_mov_b32_e32 v241, 0xdf
	v_min_f32_e32 v209, v38, v41
	v_max_f32_e32 v210, v38, v41
	v_add_f32_e32 v38, v36, v182
	v_cmp_gt_i32_e32 vcc, 0, v38
	v_mov_b32_e32 v41, 0x42
	v_mov_b32_e32 v244, 0xcf
	v_cndmask_b32_e64 v39, v39, 50, vcc
	v_and_or_b32 v40, v38, s12, v39
	v_pk_add_f32 v[38:39], v[36:37], v[36:37] op_sel:[1,0] op_sel_hi:[0,1]
	v_cmp_gt_i32_e32 vcc, 0, v38
	v_mov_b32_e32 v39, 0xbd
	v_and_b32_e32 v47, 0xffffff80, v8
	v_cndmask_b32_e32 v39, v39, v41, vcc
	v_and_or_b32 v41, v38, s12, v39
	v_pk_add_f32 v[38:39], v[48:49], v[34:35]
	v_pk_add_f32 v[48:49], v[48:49], v[32:33]
	v_cmp_gt_i32_e32 vcc, 0, v38
	v_mov_b32_e32 v39, 0xfe
	s_mov_b32 s28, 0xff61b1e6
	v_cndmask_b32_e64 v39, v39, 1, vcc
	v_and_or_b32 v211, v38, s12, v39
	v_add_f32_e32 v38, v34, v44
	v_cmp_gt_i32_e32 vcc, 0, v38
	v_mov_b32_e32 v39, 0xee
	v_add_f32_e32 v44, v32, v44
	v_cndmask_b32_e64 v39, v39, 17, vcc
	v_and_or_b32 v212, v38, s12, v39
	v_add_f32_e32 v38, v34, v46
	v_cmp_gt_i32_e32 vcc, 0, v38
	v_mov_b32_e32 v39, 0xde
	v_add_f32_e32 v46, v32, v46
	v_cndmask_b32_e64 v39, v39, 33, vcc
	v_and_or_b32 v213, v38, s12, v39
	v_add_f32_e32 v38, v34, v182
	v_cmp_gt_i32_e32 vcc, 0, v38
	v_mov_b32_e32 v39, 0xce
	v_add_f32_e32 v182, v32, v182
	v_cndmask_b32_e64 v39, v39, 49, vcc
	v_and_or_b32 v38, v38, s12, v39
	v_cmp_gt_i32_e64 s[74:75], 0, v46
	v_cmp_gt_i32_e64 s[84:85], 0, v182
	v_min_f32_e32 v219, v38, v40
	v_max_f32_e32 v220, v38, v40
	v_pk_add_f32 v[38:39], v[36:37], v[34:35] op_sel:[1,0] op_sel_hi:[0,1]
	v_cmp_gt_i32_e32 vcc, 0, v38
	v_mov_b32_e32 v39, 0xbe
	v_mov_b32_e32 v40, 0x41
	v_cndmask_b32_e32 v39, v39, v40, vcc
	v_and_or_b32 v38, v38, s12, v39
	v_mov_b32_e32 v40, v35
	v_cndmask_b32_e64 v241, v241, 32, s[74:75]
	v_min_f32_e32 v215, v38, v41
	v_max_f32_e32 v216, v38, v41
	v_pk_add_f32 v[38:39], v[34:35], v[42:43]
	v_mov_b32_e32 v41, v43
	v_pk_add_f32 v[40:41], v[34:35], v[40:41] op_sel_hi:[0,1]
	v_cmp_gt_i32_e32 vcc, 0, v38
	v_mov_b32_e32 v34, 0xae
	v_mov_b32_e32 v39, 0x51
	v_cndmask_b32_e32 v34, v34, v39, vcc
	v_cmp_gt_i32_e32 vcc, 0, v41
	v_mov_b32_e32 v39, 0x9e
	v_and_b32_e32 v38, 0xffffff00, v38
	v_cndmask_b32_e32 v39, v39, v45, vcc
	v_or_b32_e32 v218, v34, v38
	v_cmp_gt_i32_e32 vcc, 0, v40
	v_mov_b32_e32 v34, 0x8e
	v_mov_b32_e32 v38, 0x71
	v_cndmask_b32_e32 v34, v34, v38, vcc
	v_and_or_b32 v214, v40, s12, v34
	v_cmp_gt_i32_e32 vcc, 0, v48
	v_mov_b32_e32 v34, 0xff
	v_cndmask_b32_e64 v244, v244, 48, s[84:85]
	v_cndmask_b32_e64 v34, v34, 0, vcc
	v_and_or_b32 v34, v48, s12, v34
	v_and_or_b32 v46, v46, s12, v241
	v_and_or_b32 v182, v182, s12, v244
	v_max_f32_e32 v48, v34, v211
	v_min_f32_e32 v34, v34, v211
	v_max_f32_e32 v49, v48, v183
	v_max_f32_e32 v211, v34, v56
	v_min_f32_e32 v48, v48, v183
	v_min_f32_e32 v34, v34, v56
	v_max_f32_e32 v221, v49, v211
	v_max_f32_e32 v56, v48, v34
	v_min_f32_e32 v49, v49, v211
	v_min_f32_e32 v34, v48, v34
	v_max_f32_e32 v222, v221, v55
	v_max_f32_e32 v183, v56, v58
	v_max_f32_e32 v211, v49, v59
	v_max_f32_e32 v48, v34, v57
	v_min_f32_e32 v55, v221, v55
	v_min_f32_e32 v56, v56, v58
	v_min_f32_e32 v49, v49, v59
	v_min_f32_e32 v34, v34, v57
	v_max_f32_e32 v241, v46, v213
	v_max_f32_e32 v58, v55, v56
	v_max_f32_e32 v57, v49, v34
	v_min_f32_e32 v55, v55, v56
	v_min_f32_e32 v34, v49, v34
	v_min_f32_e32 v46, v46, v213
	v_max_f32_e32 v244, v181, v182
	v_max_f32_e32 v49, v55, v34
	v_min_f32_e32 v34, v55, v34
	v_cmp_gt_i32_e64 s[6:7], 0, v44
	v_min_f32_e32 v181, v181, v182
	s_nop 0
	v_cndmask_b32_e64 v234, v234, 16, s[6:7]
	v_and_or_b32 v44, v44, s12, v234
	v_max_f32_e32 v234, v44, v212
	v_min_f32_e32 v44, v44, v212
	v_max_f32_e32 v235, v234, v190
	v_max_f32_e32 v212, v44, v195
	v_min_f32_e32 v190, v234, v190
	v_min_f32_e32 v44, v44, v195
	v_max_f32_e32 v242, v241, v209
	v_max_f32_e32 v213, v46, v210
	v_min_f32_e32 v245, v244, v219
	v_min_f32_e32 v182, v181, v220
	v_min_f32_e32 v209, v241, v209
	v_min_f32_e32 v46, v46, v210
	v_max_f32_e32 v219, v244, v219
	v_max_f32_e32 v181, v181, v220
	v_max_f32_e32 v59, v58, v57
	v_min_f32_e32 v57, v58, v57
	v_max_f32_e32 v236, v235, v212
	v_max_f32_e32 v195, v190, v44
	v_min_f32_e32 v212, v235, v212
	v_min_f32_e32 v44, v190, v44
	v_max_f32_e32 v243, v242, v213
	v_min_f32_e32 v246, v245, v182
	v_max_f32_e32 v210, v209, v46
	v_min_f32_e32 v220, v219, v181
	v_min_f32_e32 v213, v242, v213
	v_max_f32_e32 v182, v245, v182
	v_min_f32_e32 v46, v209, v46
	v_max_f32_e32 v181, v219, v181
	v_max_f32_e32 v237, v236, v178
	v_max_f32_e32 v234, v195, v179
	v_max_f32_e32 v235, v212, v50
	v_max_f32_e32 v190, v44, v180
	v_min_f32_e32 v247, v243, v246
	v_min_f32_e32 v241, v210, v220
	v_min_f32_e32 v242, v213, v182
	v_min_f32_e32 v209, v46, v181
	v_min_f32_e32 v178, v236, v178
	v_min_f32_e32 v179, v195, v179
	v_min_f32_e32 v50, v212, v50
	v_min_f32_e32 v44, v44, v180
	v_max_f32_e32 v236, v243, v246
	v_max_f32_e32 v210, v210, v220
	v_max_f32_e32 v182, v213, v182
	v_max_f32_e32 v46, v46, v181
	v_max_f32_e32 v223, v222, v183
	v_max_f32_e32 v224, v211, v48
	v_min_f32_e32 v183, v222, v183
	v_min_f32_e32 v48, v211, v48
	v_max_f32_e32 v238, v237, v234
	v_max_f32_e32 v239, v235, v190
	v_min_f32_e32 v244, v247, v241
	v_min_f32_e32 v219, v242, v209
	v_max_f32_e32 v195, v178, v179
	v_max_f32_e32 v180, v50, v44
	v_min_f32_e32 v220, v236, v210
	v_min_f32_e32 v181, v182, v46
	v_min_f32_e32 v234, v237, v234
	v_min_f32_e32 v190, v235, v190
	v_max_f32_e32 v237, v247, v241
	v_max_f32_e32 v209, v242, v209
	v_min_f32_e32 v178, v178, v179
	v_min_f32_e32 v44, v50, v44
	v_max_f32_e32 v50, v236, v210
	v_max_f32_e32 v46, v182, v46
	v_max_f32_e32 v225, v223, v224
	v_max_f32_e32 v211, v183, v48
	v_min_f32_e32 v223, v223, v224
	v_min_f32_e32 v48, v183, v48
	v_max_f32_e32 v240, v238, v239
	v_min_f32_e32 v245, v244, v219
	v_max_f32_e32 v212, v195, v180
	v_min_f32_e32 v213, v220, v181
	v_max_f32_e32 v235, v234, v190
	v_min_f32_e32 v241, v237, v209
	v_max_f32_e32 v179, v178, v44
	v_min_f32_e32 v182, v50, v46
	v_min_f32_e32 v238, v238, v239
	v_max_f32_e32 v219, v244, v219
	v_min_f32_e32 v180, v195, v180
	v_max_f32_e32 v181, v220, v181
	v_min_f32_e32 v190, v234, v190
	v_max_f32_e32 v209, v237, v209
	v_min_f32_e32 v44, v178, v44
	v_max_f32_e32 v46, v50, v46
	v_max_f32_e32 v226, v225, v51
	v_max_f32_e32 v221, v59, v173
	v_max_f32_e32 v222, v211, v60
	v_max_f32_e32 v56, v49, v61
	v_max_f32_e32 v224, v223, v62
	v_max_f32_e32 v58, v57, v63
	v_max_f32_e32 v183, v48, v52
	v_max_f32_e32 v55, v34, v53
	v_min_f32_e32 v248, v240, v245
	v_min_f32_e32 v243, v212, v213
	v_min_f32_e32 v242, v235, v241
	v_min_f32_e32 v210, v179, v182
	v_min_f32_e32 v239, v238, v219
	v_min_f32_e32 v195, v180, v181
	v_min_f32_e32 v234, v190, v209
	v_min_f32_e32 v178, v44, v46
	v_max_f32_e32 v227, v226, v221
	v_max_f32_e32 v228, v222, v56
	v_max_f32_e32 v230, v224, v58
	v_max_f32_e32 v231, v183, v55
	v_min_f32_e32 v246, v248, v243
	v_min_f32_e32 v236, v242, v210
	v_min_f32_e32 v220, v239, v195
	v_min_f32_e32 v237, v234, v178
	v_max_f32_e32 v229, v227, v228
	v_max_f32_e32 v232, v230, v231
	v_min_f32_e32 v247, v246, v236
	v_min_f32_e32 v244, v220, v237
	v_min_f32_e32 v51, v225, v51
	v_min_f32_e32 v59, v59, v173
	v_min_f32_e32 v60, v211, v60
	v_min_f32_e32 v61, v49, v61
	v_min_f32_e32 v62, v223, v62
	v_min_f32_e32 v57, v57, v63
	v_min_f32_e32 v48, v48, v52
	v_min_f32_e32 v34, v34, v53
	v_max_f32_e32 v63, v240, v245
	v_max_f32_e32 v212, v212, v213
	v_max_f32_e32 v235, v235, v241
	v_max_f32_e32 v179, v179, v182
	v_max_f32_e32 v219, v238, v219
	v_max_f32_e32 v180, v180, v181
	v_max_f32_e32 v190, v190, v209
	v_max_f32_e32 v44, v44, v46
	v_max_f32_e32 v233, v229, v232
	v_min_f32_e32 v50, v247, v244
	v_max_f32_e32 v173, v51, v59
	v_max_f32_e32 v211, v60, v61
	v_max_f32_e32 v223, v62, v57
	v_max_f32_e32 v53, v48, v34
	v_min_f32_e32 v213, v63, v212
	v_min_f32_e32 v182, v235, v179
	v_min_f32_e32 v181, v219, v180
	v_min_f32_e32 v46, v190, v44
	v_min_f32_e32 v227, v227, v228
	v_min_f32_e32 v228, v230, v231
	v_max_f32_e32 v230, v246, v236
	v_max_f32_e32 v220, v220, v237
	v_max_f32_e32 v50, v233, v50
	v_max_f32_e32 v44, v190, v44
	v_max_f32_e32 v225, v173, v211
	v_max_f32_e32 v233, v223, v53
	v_min_f32_e32 v240, v213, v182
	v_min_f32_e32 v209, v181, v46
	v_min_f32_e32 v221, v226, v221
	v_min_f32_e32 v222, v222, v56
	v_min_f32_e32 v224, v224, v58
	v_min_f32_e32 v183, v183, v55
	v_max_f32_e32 v241, v248, v243
	v_max_f32_e32 v210, v242, v210
	v_max_f32_e32 v195, v239, v195
	v_max_f32_e32 v234, v234, v178
	v_min_f32_e32 v51, v51, v59
	v_min_f32_e32 v59, v60, v61
	v_min_f32_e32 v57, v62, v57
	v_min_f32_e32 v34, v48, v34
	v_max_f32_e32 v60, v63, v212
	v_max_f32_e32 v62, v235, v179
	v_max_f32_e32 v58, v227, v228
	v_min_f32_e32 v63, v230, v220
	v_min_f32_e32 v211, v173, v211
	v_min_f32_e32 v223, v223, v53
	v_max_f32_e32 v213, v213, v182
	v_max_f32_e32 v46, v181, v46
	v_max_f32_e32 v226, v221, v222
	v_max_f32_e32 v238, v224, v183
	v_max_f32_e32 v243, v51, v59
	v_max_f32_e32 v245, v57, v34
	v_min_f32_e32 v179, v60, v62
	v_max_f32_e32 v63, v58, v63
	v_max_f32_e32 v53, v211, v223
	v_min_f32_e32 v58, v213, v46
	v_min_f32_e32 v181, v221, v222
	v_min_f32_e32 v221, v224, v183
	v_max_f32_e32 v222, v241, v210
	v_max_f32_e32 v224, v195, v234
	v_min_f32_e32 v51, v51, v59
	v_min_f32_e32 v59, v57, v34
	v_max_f32_e32 v231, v60, v62
	v_min_f32_e32 v57, v229, v232
	v_max_f32_e32 v62, v247, v244
	v_min_f32_e32 v239, v195, v234
	v_min_f32_e32 v242, v241, v210
	v_max_f32_e32 v212, v219, v180
	v_max_f32_e32 v178, v53, v58
	v_max_f32_e32 v53, v181, v221
	v_min_f32_e32 v173, v222, v224
	v_max_f32_e32 v183, v57, v62
	v_min_f32_e32 v57, v225, v233
	v_max_f32_e32 v62, v240, v209
	v_min_f32_e32 v219, v212, v44
	v_max_f32_e32 v180, v53, v173
	v_max_f32_e32 v190, v57, v62
	v_min_f32_e32 v57, v226, v238
	v_max_f32_e32 v173, v242, v239
	v_max_f32_e32 v55, v226, v238
	v_min_f32_e32 v56, v242, v239
	v_max_f32_e32 v210, v230, v220
	v_max_f32_e32 v195, v57, v173
	v_min_f32_e32 v57, v243, v245
	v_max_f32_e32 v173, v179, v219
	v_max_f32_e32 v55, v55, v56
	v_min_f32_e32 v56, v179, v219
	v_min_f32_e32 v179, v227, v228
	v_min_f32_e32 v52, v240, v209
	v_max_f32_e32 v209, v57, v173
	v_max_f32_e32 v46, v213, v46
	v_max_f32_e32 v44, v212, v44
	v_max_f32_e32 v210, v179, v210
	v_min_f32_e32 v179, v211, v223
	v_max_f32_e32 v211, v179, v46
	v_min_f32_e32 v46, v181, v221
	v_max_f32_e32 v181, v222, v224
	v_min_f32_e32 v53, v231, v44
	v_max_f32_e32 v44, v231, v44
	v_max_f32_e32 v212, v46, v181
	v_min_f32_e32 v46, v51, v59
	v_max_f32_e32 v34, v51, v59
	v_pk_add_f32 v[36:37], v[36:37], v[32:33] op_sel:[1,0] op_sel_hi:[0,1]
	v_mov_b32_e32 v37, 0xbf
	v_max_f32_e32 v213, v46, v44
	v_cmp_gt_i32_e32 vcc, 0, v36
	v_mov_b32_e32 v221, 0x50
	v_and_b32_e32 v41, 0xffffff00, v41
	v_cndmask_b32_e64 v37, v37, 64, vcc
	v_and_or_b32 v36, v36, s12, v37
	v_or_b32_e32 v217, v39, v41
	v_max_f32_e32 v49, v225, v233
	v_max_f32_e32 v44, v54, v36
	v_min_f32_e32 v54, v54, v36
	v_pk_add_f32 v[36:37], v[32:33], v[42:43] op_sel_hi:[0,1]
	v_cmp_gt_i32_e64 s[68:69], 0, v37
	v_mov_b32_e32 v42, 0x9f
	v_mov_b32_e32 v43, 0x60
	v_cndmask_b32_e64 v42, v42, v43, s[68:69]
	v_cmp_gt_i32_e64 s[68:69], 0, v36
	v_mov_b32_e32 v43, 0xaf
	v_and_b32_e32 v37, 0xffffff00, v37
	v_cndmask_b32_e64 v43, v43, v221, s[68:69]
	v_and_b32_e32 v36, 0xffffff00, v36
	v_or_b32_e32 v37, v42, v37
	v_or_b32_e32 v36, v43, v36
	v_min_f32_e32 v42, v37, v217
	v_max_f32_e32 v43, v36, v218
	v_max_f32_e32 v37, v37, v217
	v_min_f32_e32 v36, v36, v218
	v_max_f32_e32 v46, v44, v215
	v_max_f32_e32 v219, v54, v216
	v_min_f32_e32 v221, v43, v42
	v_min_f32_e32 v217, v36, v37
	v_max_f32_e32 v42, v43, v42
	v_max_f32_e32 v36, v36, v37
	v_max_f32_e32 v220, v46, v219
	v_min_f32_e32 v44, v44, v215
	v_min_f32_e32 v54, v54, v216
	v_min_f32_e32 v219, v46, v219
	v_mov_b32_e32 v46, v35
	v_min_f32_e32 v216, v42, v36
	v_max_f32_e32 v225, v42, v36
	v_pk_add_f32 v[36:37], v[32:33], v[46:47] op_sel_hi:[0,1]
	v_and_b32_e32 v45, 0xffffff80, v9
	v_max_f32_e32 v215, v44, v54
	v_min_f32_e32 v54, v44, v54
	v_mov_b32_e32 v44, v35
	v_cmp_gt_i32_e32 vcc, 0, v37
	v_mov_b32_e32 v35, 0x7f
	v_pk_add_f32 v[42:43], v[32:33], v[44:45] op_sel_hi:[0,1]
	v_cndmask_b32_e32 v35, v35, v196, vcc
	v_cmp_gt_i32_e32 vcc, 0, v36
	v_mov_b32_e32 v47, 0x8f
	v_mov_b32_e32 v45, 0x6f
	v_cndmask_b32_e32 v44, v47, v198, vcc
	v_cmp_gt_i32_e32 vcc, 0, v43
	v_mov_b32_e32 v46, 0x90
	v_and_b32_e32 v37, 0xffffff00, v37
	v_and_b32_e32 v36, 0xffffff00, v36
	v_cndmask_b32_e32 v45, v45, v46, vcc
	v_and_b32_e32 v43, 0xffffff00, v43
	v_cmp_gt_i32_e32 vcc, 0, v42
	v_or_b32_e32 v35, v35, v37
	v_or_b32_e32 v36, v44, v36
	v_or_b32_e32 v37, v45, v43
	v_and_b32_e32 v41, 0xffffff80, v10
	v_and_b32_e32 v40, 0xffffff80, v13
	v_cndmask_b32_e32 v46, v47, v198, vcc
	v_cmp_lt_f32_e32 vcc, v37, v35
	v_cmp_lt_f32_e64 s[8:9], v214, v36
	v_and_b32_e32 v39, 0xffffff80, v12
	v_cndmask_b32_e32 v43, v35, v37, vcc
	v_cndmask_b32_e64 v45, v36, v214, s[8:9]
	v_cndmask_b32_e32 v35, v37, v35, vcc
	v_pk_add_f32 v[36:37], v[32:33], v[40:41] op_sel_hi:[0,1]
	v_cmp_gt_i32_e64 s[80:81], 0, v37
	v_mov_b32_e32 v40, 0x5f
	v_mov_b32_e32 v41, 0xa0
	v_and_b32_e32 v38, 0xffffff80, v11
	v_cndmask_b32_e64 v40, v40, v41, s[80:81]
	v_and_b32_e32 v42, 0xffffff00, v42
	v_and_or_b32 v37, v37, s12, v40
	v_cmp_gt_i32_e64 s[80:81], 0, v36
	v_mov_b32_e32 v40, 0xd0
	v_pk_add_f32 v[38:39], v[32:33], v[38:39] op_sel_hi:[0,1]
	v_or_b32_e32 v42, v46, v42
	v_cndmask_b32_e64 v40, 47, v40, s[80:81]
	v_cmp_gt_i32_e64 s[80:81], 0, v39
	v_mov_b32_e32 v41, 0xc0
	v_cndmask_b32_e64 v42, v214, v42, s[8:9]
	v_cndmask_b32_e64 v41, 63, v41, s[80:81]
	v_cmp_gt_i32_e64 s[80:81], 0, v38
	v_mov_b32_e32 v214, 0x4f
	v_mov_b32_e32 v229, 0xb0
	v_cndmask_b32_e64 v214, v214, v229, s[80:81]
	v_and_b32_e32 v39, 0xffffff00, v39
	v_and_b32_e32 v38, 0xffffff00, v38
	v_and_b32_e32 v36, 0xffffff00, v36
	v_or_b32_e32 v39, v41, v39
	v_or_b32_e32 v38, v214, v38
	v_or_b32_e32 v36, v40, v36
	v_min_f32_e32 v40, v39, v36
	v_max_f32_e32 v41, v37, v38
	v_min_f32_e32 v37, v37, v38
	v_max_f32_e32 v36, v39, v36
	v_max_f32_e32 v44, v42, v43
	v_max_f32_e32 v46, v45, v35
	v_min_f32_e32 v214, v41, v40
	v_min_f32_e32 v38, v37, v36
	v_min_f32_e32 v42, v42, v43
	v_min_f32_e32 v35, v45, v35
	v_max_f32_e32 v40, v41, v40
	v_max_f32_e32 v36, v37, v36
	v_max_f32_e32 v47, v44, v46
	v_min_f32_e32 v39, v214, v38
	v_max_f32_e32 v43, v42, v35
	v_min_f32_e32 v37, v40, v36
	v_min_f32_e32 v44, v44, v46
	v_max_f32_e32 v38, v214, v38
	v_min_f32_e32 v35, v42, v35
	v_max_f32_e32 v36, v40, v36
	v_min_f32_e32 v218, v221, v217
	v_max_f32_e32 v217, v221, v217
	v_min_f32_e32 v229, v47, v39
	v_min_f32_e32 v41, v43, v37
	v_min_f32_e32 v46, v44, v38
	v_min_f32_e32 v40, v35, v36
	v_max_f32_e32 v39, v47, v39
	v_max_f32_e32 v37, v43, v37
	v_max_f32_e32 v38, v44, v38
	v_max_f32_e32 v35, v35, v36
	v_max_f32_e32 v222, v220, v218
	v_max_f32_e32 v223, v215, v216
	v_max_f32_e32 v221, v219, v217
	v_max_f32_e32 v226, v54, v225
	v_min_f32_e32 v218, v220, v218
	v_min_f32_e32 v215, v215, v216
	v_min_f32_e32 v217, v219, v217
	v_min_f32_e32 v54, v54, v225
	v_min_f32_e32 v43, v39, v37
	v_min_f32_e32 v36, v38, v35
	v_max_f32_e32 v37, v39, v37
	v_max_f32_e32 v35, v38, v35
	v_max_f32_e32 v216, v218, v215
	v_max_f32_e32 v219, v217, v54
	v_min_f32_e32 v44, v43, v36
	v_min_f32_e32 v215, v218, v215
	v_min_f32_e32 v54, v217, v54
	v_min_f32_e32 v38, v37, v35
	v_max_f32_e32 v43, v43, v36
	v_max_f32_e32 v35, v37, v35
	v_and_b32_e32 v37, 0xffffff80, v15
	v_mov_b32_e32 v36, v33
	v_pk_add_f32 v[32:33], v[32:33], v[36:37] op_sel_hi:[0,1]
	v_mov_b32_e32 v37, 0xe0
	v_max_f32_e32 v217, v215, v54
	v_min_f32_e32 v54, v215, v54
	v_cmp_gt_i32_e64 s[76:77], 0, v33
	v_and_b32_e32 v33, 0xffffff00, v33
	s_nop 0
	v_cndmask_b32_e64 v36, 15, v249, s[76:77]
	v_cmp_gt_i32_e64 s[76:77], 0, v32
	v_and_b32_e32 v32, 0xffffff00, v32
	v_or_b32_e32 v33, v36, v33
	v_cndmask_b32_e64 v37, 31, v37, s[76:77]
	v_or_b32_e32 v32, v37, v32
	v_max_f32_e32 v36, v32, v33
	v_min_f32_e32 v32, v32, v33
	v_max_f32_e32 v37, v36, v36
	v_max_f32_e32 v33, v32, v32
	v_max_f32_e32 v37, 0xff61b1e6, v37
	v_max_f32_e32 v33, 0xff61b1e6, v33
	v_max_f32_e32 v224, v222, v223
	v_max_f32_e32 v233, v37, v33
	v_min_f32_e32 v33, v37, v33
	v_max_f32_e32 v234, 0xff61b1e6, v233
	v_max_f32_e32 v37, 0xff61b1e6, v33
	v_cmp_nlt_f32_e32 vcc, s28, v33
	v_max_f32_e32 v227, v221, v226
	v_max_f32_e32 v235, v234, v37
	v_cmp_nlt_f32_e64 s[88:89], s28, v235
	v_cndmask_b32_e32 v33, v199, v33, vcc
	v_min_f32_e32 v45, v229, v41
	v_cndmask_b32_e64 v236, v199, v235, s[88:89]
	v_cmp_nlt_f32_e64 s[88:89], s28, v233
	v_min_f32_e32 v42, v46, v40
	v_min_f32_e32 v222, v222, v223
	v_cndmask_b32_e64 v233, v199, v233, s[88:89]
	v_cmp_nlt_f32_e64 s[88:89], s28, v36
	v_min_f32_e32 v221, v221, v226
	v_max_f32_e32 v41, v229, v41
	v_cndmask_b32_e64 v36, v199, v36, s[88:89]
	v_cmp_nlt_f32_e64 s[88:89], s28, v32
	v_max_f32_e32 v40, v46, v40
	s_nop 0
	v_cndmask_b32_e64 v32, v199, v32, s[88:89]
	v_max_f32_e32 v237, v36, v32
	v_min_f32_e32 v32, v36, v32
	v_max_f32_e32 v238, v233, v237
	v_max_f32_e32 v36, v33, v32
	v_max_f32_e32 v228, v224, v227
	v_min_f32_e32 v214, v45, v42
	v_max_f32_e32 v220, v216, v219
	v_max_f32_e32 v223, v222, v221
	v_min_f32_e32 v46, v41, v40
	v_min_f32_e32 v224, v224, v227
	v_max_f32_e32 v42, v45, v42
	v_min_f32_e32 v216, v216, v219
	v_min_f32_e32 v221, v222, v221
	v_max_f32_e32 v40, v41, v40
	v_max_f32_e32 v239, v238, v36
	v_min_f32_e32 v233, v233, v237
	v_min_f32_e32 v32, v33, v32
	v_min_f32_e32 v37, v234, v37
	v_min_f32_e32 v36, v238, v36
	v_max_f32_e32 v52, v49, v52
	s_mov_b64 s[6:7], s[96:97]
	v_cmp_nlt_f32_e64 s[88:89], s28, v239
	v_cmp_nlt_f32_e64 s[76:77], s28, v37
	v_cmp_nlt_f32_e64 s[14:15], s28, v36
	v_max_f32_e32 v230, v228, v214
	v_max_f32_e32 v47, v220, v44
	v_max_f32_e32 v226, v223, v46
	v_max_f32_e32 v39, v217, v38
	v_max_f32_e32 v45, v224, v42
	v_max_f32_e32 v219, v216, v43
	v_max_f32_e32 v41, v221, v40
	v_max_f32_e32 v215, v54, v35
	v_cndmask_b32_e64 v240, v199, v239, s[88:89]
	v_max_f32_e32 v33, v233, v32
	v_cndmask_b32_e64 v234, v199, v37, s[76:77]
	v_cndmask_b32_e64 v238, v199, v36, s[14:15]
	v_min_f32_e32 v32, v233, v32
	v_cmp_nlt_f32_e64 s[88:89], s28, v33
	v_cmp_nlt_f32_e32 vcc, s28, v32
	v_max_f32_e32 v48, v243, v245
	v_max_f32_e32 v225, v230, v47
	v_max_f32_e32 v218, v226, v39
	v_max_f32_e32 v227, v45, v219
	v_max_f32_e32 v222, v41, v215
	v_min_f32_e32 v241, v236, v240
	v_cndmask_b32_e64 v237, v199, v33, s[88:89]
	v_min_f32_e32 v243, v234, v238
	v_cndmask_b32_e32 v233, v199, v32, vcc
	v_max_f32_e32 v229, v225, v218
	v_max_f32_e32 v231, v227, v222
	v_min_f32_e32 v242, v241, v237
	v_min_f32_e32 v244, v243, v233
	v_min_f32_e32 v214, v228, v214
	v_max_f32_e32 v232, v229, v231
	v_min_f32_e32 v245, v242, v244
	v_max_f32_e32 v228, 0xff61b1e6, v235
	v_max_f32_e32 v235, v239, v239
	v_max_f32_e32 v36, v36, v36
	v_min_f32_e32 v44, v220, v44
	v_min_f32_e32 v46, v223, v46
	v_min_f32_e32 v38, v217, v38
	v_min_f32_e32 v42, v224, v42
	v_min_f32_e32 v43, v216, v43
	v_min_f32_e32 v40, v221, v40
	v_min_f32_e32 v35, v54, v35
	v_max_f32_e32 v235, 0xff61b1e6, v235
	v_max_f32_e32 v33, v33, v33
	v_max_f32_e32 v37, 0xff61b1e6, v37
	v_max_f32_e32 v36, 0xff61b1e6, v36
	v_max_f32_e32 v32, v32, v32
	v_max_f32_e32 v232, v232, v245
	s_mov_b32 s36, s18
	v_max_f32_e32 v33, 0xff61b1e6, v33
	v_max_f32_e32 v32, 0xff61b1e6, v32
	v_max_f32_e32 v220, v214, v44
	v_max_f32_e32 v217, v46, v38
	v_max_f32_e32 v216, v42, v43
	v_max_f32_e32 v54, v40, v35
	v_min_f32_e32 v239, v228, v235
	v_min_f32_e32 v245, 0xff61b1e6, v33
	v_min_f32_e32 v247, v37, v36
	v_min_f32_e32 v248, 0xff61b1e6, v32
	v_max_f32_e32 v223, v220, v217
	v_max_f32_e32 v221, v216, v54
	v_min_f32_e32 v246, v239, v245
	v_min_f32_e32 v249, v247, v248
	v_min_f32_e32 v47, v230, v47
	v_max_f32_e32 v230, v236, v240
	v_cmp_ngt_f32_e64 s[16:17], s28, v237
	v_max_f32_e32 v234, v234, v238
	v_cmp_ngt_f32_e64 s[14:15], s28, v233
	v_min_f32_e32 v44, v214, v44
	v_min_f32_e32 v38, v46, v38
	v_min_f32_e32 v42, v42, v43
	v_min_f32_e32 v35, v40, v35
	v_max_f32_e32 v214, v228, v235
	v_max_f32_e32 v36, v37, v36
	v_max_f32_e32 v224, v223, v221
	v_min_f32_e32 v250, v246, v249
	v_min_f32_e32 v39, v226, v39
	v_min_f32_e32 v45, v45, v219
	v_min_f32_e32 v41, v41, v215
	v_cndmask_b32_e64 v236, v199, v237, s[16:17]
	v_cndmask_b32_e64 v238, v199, v233, s[14:15]
	v_max_f32_e32 v46, v44, v38
	v_max_f32_e32 v40, v42, v35
	v_min_f32_e32 v228, v214, v33
	v_min_f32_e32 v37, v36, v32
	v_max_f32_e32 v224, v224, v250
	v_max_f32_e32 v226, v47, v39
	v_max_f32_e32 v215, v45, v41
	v_min_f32_e32 v240, v230, v236
	v_min_f32_e32 v250, v234, v238
	v_min_f32_e32 v218, v225, v218
	v_min_f32_e32 v222, v227, v222
	v_max_f32_e32 v237, v241, v237
	v_max_f32_e32 v233, v243, v233
	v_min_f32_e32 v39, v47, v39
	v_min_f32_e32 v41, v45, v41
	v_max_f32_e32 v47, v230, v236
	v_max_f32_e32 v230, v234, v238
	v_max_f32_e32 v43, v46, v40
	v_min_f32_e32 v235, v228, v37
	v_min_f32_e32 v217, v220, v217
	v_min_f32_e32 v54, v216, v54
	v_max_f32_e32 v239, v239, v245
	v_max_f32_e32 v243, v247, v248
	v_min_f32_e32 v38, v44, v38
	v_min_f32_e32 v35, v42, v35
	v_max_f32_e32 v33, v214, v33
	v_max_f32_e32 v32, v36, v32
	v_max_f32_e32 v219, v226, v215
	v_max_f32_e32 v227, v218, v222
	v_min_f32_e32 v241, v237, v233
	v_max_f32_e32 v45, v39, v41
	v_min_f32_e32 v234, v47, v230
	v_min_f32_e32 v229, v229, v231
	v_max_f32_e32 v231, v242, v244
	v_min_f32_e32 v215, v226, v215
	v_max_f32_e32 v226, v240, v250
	v_min_f32_e32 v251, v240, v250
	v_max_f32_e32 v43, v43, v235
	v_max_f32_e32 v216, v217, v54
	v_min_f32_e32 v245, v239, v243
	v_max_f32_e32 v42, v38, v35
	v_min_f32_e32 v36, v33, v32
	v_min_f32_e32 v221, v223, v221
	v_max_f32_e32 v223, v246, v249
	v_min_f32_e32 v40, v46, v40
	v_max_f32_e32 v37, v228, v37
	v_min_f32_e32 v218, v218, v222
	v_max_f32_e32 v222, v237, v233
	v_min_f32_e32 v54, v217, v54
	v_max_f32_e32 v217, v239, v243
	v_min_f32_e32 v39, v39, v41
	v_max_f32_e32 v41, v47, v230
	v_min_f32_e32 v35, v38, v35
	v_max_f32_e32 v32, v33, v32
	v_max_f32_e32 v227, v227, v241
	v_max_f32_e32 v45, v45, v234
	v_max_f32_e32 v229, v229, v231
	v_max_f32_e32 v215, v215, v226
	v_max_f32_e32 v61, v48, v56
	v_max_f32_e32 v182, v34, v53
	v_max_f32_e32 v219, v219, v251
	v_max_f32_e32 v216, v216, v245
	v_max_f32_e32 v36, v42, v36
	v_max_f32_e32 v221, v221, v223
	v_max_f32_e32 v37, v40, v37
	v_max_f32_e32 v218, v218, v222
	v_max_f32_e32 v217, v54, v217
	v_max_f32_e32 v39, v39, v41
	v_max_f32_e32 v32, v35, v32
	v_max_f32_e32 v49, v50, v52
	v_max_f32_e32 v56, v55, v61
	v_max_f32_e32 v58, v63, v178
	v_max_f32_e32 v60, v180, v182
	v_max_f32_e32 v62, v183, v190
	v_max_f32_e32 v173, v195, v209
	v_max_f32_e32 v179, v210, v211
	v_max_f32_e32 v181, v212, v213
	v_min_f32_e32 v225, v232, v224
	v_min_f32_e32 v241, v219, v43
	v_min_f32_e32 v245, v227, v216
	v_min_f32_e32 v42, v45, v36
	v_min_f32_e32 v223, v229, v221
	v_min_f32_e32 v40, v215, v37
	v_min_f32_e32 v222, v218, v217
	v_min_f32_e32 v33, v39, v32
	v_max_f32_e32 v48, v49, v56
	v_max_f32_e32 v53, v58, v60
	v_max_f32_e32 v57, v62, v173
	v_max_f32_e32 v59, v179, v181
	v_min_f32_e32 v220, v225, v241
	v_min_f32_e32 v44, v245, v42
	v_min_f32_e32 v46, v223, v40
	v_min_f32_e32 v35, v222, v33
	v_max_f32_e32 v34, v48, v53
	v_max_f32_e32 v51, v57, v59
	v_min_f32_e32 v214, v220, v44
	v_min_f32_e32 v38, v46, v35
	v_min_f32_e32 v47, v55, v61
	v_max_f32_e32 v235, v34, v51
	v_min_f32_e32 v41, v214, v38
	v_min_f32_e32 v61, v63, v178
	v_min_f32_e32 v63, v180, v182
	v_max_f32_e32 v54, v235, v41
	v_min_f32_e32 v41, v50, v52
	v_min_f32_e32 v182, v183, v190
	v_min_f32_e32 v183, v195, v209
	v_min_f32_e32 v190, v210, v211
	v_min_f32_e32 v209, v212, v213
	v_max_f32_e32 v212, v232, v224
	v_max_f32_e32 v43, v219, v43
	v_max_f32_e32 v216, v227, v216
	v_max_f32_e32 v36, v45, v36
	v_max_f32_e32 v221, v229, v221
	v_max_f32_e32 v37, v215, v37
	v_max_f32_e32 v217, v218, v217
	v_max_f32_e32 v32, v39, v32
	v_min_f32_e32 v49, v49, v56
	v_min_f32_e32 v224, v58, v60
	v_min_f32_e32 v62, v62, v173
	v_min_f32_e32 v173, v179, v181
	v_max_f32_e32 v181, v225, v241
	v_max_f32_e32 v42, v245, v42
	v_max_f32_e32 v40, v223, v40
	v_max_f32_e32 v33, v222, v33
	v_max_f32_e32 v50, v41, v47
	v_max_f32_e32 v178, v61, v63
	v_max_f32_e32 v195, v182, v183
	v_min_f32_e32 v213, v212, v43
	v_min_f32_e32 v45, v216, v36
	v_min_f32_e32 v215, v221, v37
	v_min_f32_e32 v39, v217, v32
	v_max_f32_e32 v226, v49, v224
	v_max_f32_e32 v179, v62, v173
	v_min_f32_e32 v225, v181, v42
	v_min_f32_e32 v222, v40, v33
	v_min_f32_e32 v41, v41, v47
	v_min_f32_e32 v47, v61, v63
	v_min_f32_e32 v63, v182, v183
	v_min_f32_e32 v182, v190, v209
	v_max_f32_e32 v43, v212, v43
	v_max_f32_e32 v36, v216, v36
	v_max_f32_e32 v37, v221, v37
	v_max_f32_e32 v32, v217, v32
	v_cmp_gt_f32_e64 s[24:25], v63, v182
	v_max_f32_e32 v210, v190, v209
	v_max_f32_e32 v56, v226, v179
	v_min_f32_e32 v58, v225, v222
	v_max_f32_e32 v223, v41, v47
	v_cndmask_b32_e64 v183, v182, v63, s[24:25]
	v_min_f32_e32 v209, v43, v36
	v_min_f32_e32 v212, v37, v32
	v_max_f32_e32 v56, v56, v58
	v_max_f32_e32 v58, v223, v183
	v_min_f32_e32 v60, v209, v212
	v_min_f32_e32 v48, v48, v53
	v_min_f32_e32 v217, v57, v59
	v_max_f32_e32 v44, v220, v44
	v_max_f32_e32 v35, v46, v35
	v_max_f32_e32 v58, v58, v60
	v_max_f32_e32 v53, v48, v217
	v_min_f32_e32 v46, v44, v35
	v_max_f32_e32 v180, v50, v178
	v_min_f32_e32 v219, v213, v45
	v_min_f32_e32 v218, v215, v39
	v_max_f32_e32 v59, v53, v46
	v_min_f32_e32 v46, v50, v178
	v_min_f32_e32 v50, v195, v210
	v_max_f32_e32 v45, v213, v45
	v_max_f32_e32 v39, v215, v39
	v_min_f32_e32 v49, v49, v224
	v_max_f32_e32 v53, v46, v50
	v_min_f32_e32 v57, v45, v39
	v_min_f32_e32 v213, v62, v173
	v_max_f32_e32 v42, v181, v42
	v_max_f32_e32 v33, v40, v33
	v_max_f32_e32 v60, v53, v57
	v_cmp_gt_f32_e64 s[20:21], v49, v213
	v_max_f32_e32 v211, v195, v210
	s_nop 0
	v_cndmask_b32_e64 v57, v213, v49, s[20:21]
	v_min_f32_e32 v40, v42, v33
	v_max_f32_e32 v36, v43, v36
	v_max_f32_e32 v32, v37, v32
	v_max_f32_e32 v61, v57, v40
	v_min_f32_e32 v40, v41, v47
	v_cndmask_b32_e64 v41, v63, v182, s[24:25]
	v_cmp_gt_f32_e64 s[14:15], v40, v41
	v_min_f32_e32 v34, v34, v51
	s_nop 0
	v_cndmask_b32_e64 v47, v41, v40, s[14:15]
	v_min_f32_e32 v37, v36, v32
	s_mov_b64 s[96:97], s[6:7]
	v_max_f32_e32 v62, v47, v37
	v_max_f32_e32 v37, v214, v38
	v_max_f32_e32 v35, v44, v35
	v_min_f32_e32 v55, v219, v218
	v_max_f32_e32 v63, v34, v37
	v_min_f32_e32 v34, v180, v211
	v_max_f32_e32 v37, v219, v218
	v_max_f32_e32 v52, v180, v211
	v_max_f32_e32 v33, v42, v33
	v_max_f32_e32 v173, v34, v37
	v_min_f32_e32 v34, v226, v179
	v_max_f32_e32 v37, v225, v222
	v_max_f32_e32 v32, v36, v32
	v_max_f32_e32 v178, v34, v37
	v_min_f32_e32 v34, v223, v183
	v_max_f32_e32 v37, v209, v212
	v_max_f32_e32 v55, v52, v55
	v_max_f32_e32 v179, v34, v37
	v_min_f32_e32 v34, v48, v217
	v_max_f32_e32 v180, v34, v35
	v_min_f32_e32 v34, v46, v50
	v_max_f32_e32 v35, v45, v39
	v_max_f32_e32 v181, v34, v35
	v_cndmask_b32_e64 v34, v49, v213, s[20:21]
	v_max_f32_e32 v182, v34, v33
	v_cndmask_b32_e64 v33, v40, v41, s[14:15]
	v_min_f32_e32 v52, v54, v55
	v_min_f32_e32 v190, v56, v58
	v_max_f32_e32 v183, v33, v32
	v_min_f32_e32 v53, v59, v60
	v_min_f32_e32 v57, v61, v62
	v_min_f32_e32 v195, v63, v173
	v_min_f32_e32 v209, v178, v179
	v_min_f32_e32 v210, v180, v181
	v_min_f32_e32 v211, v182, v183
	v_min_f32_e32 v216, v52, v190
	v_min_f32_e32 v215, v53, v57
	v_min_f32_e32 v51, v195, v209
	v_min_f32_e32 v50, v210, v211
	s_movk_i32 s10, 0xff
	v_min_f32_e32 v220, v216, v215
	v_min_f32_e32 v212, v51, v50
	s_movk_i32 s8, 0x7f
	v_bitop3_b32 v35, v31, s8, v31 bitop3:0xc
	v_min_f32_e32 v32, v220, v212
	v_and_b32_e32 v33, 0xff, v32
	v_bitop3_b32 v34, v32, s10, v32 bitop3:0xc
	v_cmp_gt_i32_e64 s[6:7], 0, v32
	v_readlane_b32 s94, v255, 39
	v_readlane_b32 s95, v255, 40
	v_cndmask_b32_e64 v213, v34, v33, s[6:7]
	v_and_b32_e32 v33, 0x7f, v31
	v_cmp_gt_i32_e64 s[6:7], 0, v31
	v_and_b32_e32 v34, 15, v213
	v_lshrrev_b32_e32 v214, 4, v213
	v_cndmask_b32_e64 v31, v35, v33, s[6:7]
	v_and_b32_e32 v33, 0x7f, v30
	v_bitop3_b32 v35, v30, s8, v30 bitop3:0xc
	v_cmp_gt_i32_e64 s[6:7], 0, v30
	v_readlane_b32 s86, v255, 31
	v_readlane_b32 s82, v255, 33
	v_cndmask_b32_e64 v30, v35, v33, s[6:7]
	v_and_b32_e32 v33, 0x7f, v29
	v_bitop3_b32 v35, v29, s8, v29 bitop3:0xc
	v_cmp_gt_i32_e64 s[6:7], 0, v29
	v_readlane_b32 s84, v255, 25
	v_readlane_b32 s87, v255, 32
	v_cndmask_b32_e64 v29, v35, v33, s[6:7]
	v_and_b32_e32 v33, 0x7f, v28
	v_bitop3_b32 v35, v28, s8, v28 bitop3:0xc
	v_cmp_gt_i32_e64 s[6:7], 0, v28
	v_readlane_b32 s92, v255, 35
	v_readlane_b32 s88, v255, 29
	v_cndmask_b32_e64 v28, v35, v33, s[6:7]
	v_and_b32_e32 v33, 0x7f, v27
	v_bitop3_b32 v35, v27, s8, v27 bitop3:0xc
	v_cmp_gt_i32_e64 s[6:7], 0, v27
	v_readlane_b32 s90, v255, 27
	v_readlane_b32 s78, v255, 13
	v_cndmask_b32_e64 v27, v35, v33, s[6:7]
	v_and_b32_e32 v33, 0x7f, v26
	v_bitop3_b32 v35, v26, s8, v26 bitop3:0xc
	v_cmp_gt_i32_e64 s[6:7], 0, v26
	v_readlane_b32 s83, v255, 34
	v_readlane_b32 s74, v255, 9
	v_cndmask_b32_e64 v26, v35, v33, s[6:7]
	v_and_b32_e32 v33, 0x7f, v25
	v_bitop3_b32 v35, v25, s8, v25 bitop3:0xc
	v_cmp_gt_i32_e64 s[6:7], 0, v25
	v_readlane_b32 s85, v255, 26
	v_readlane_b32 s76, v255, 11
	v_cndmask_b32_e64 v25, v35, v33, s[6:7]
	v_and_b32_e32 v33, 0x7f, v24
	v_bitop3_b32 v35, v24, s8, v24 bitop3:0xc
	v_cmp_gt_i32_e64 s[6:7], 0, v24
	v_readlane_b32 s22, v255, 23
	v_readlane_b32 s34, v255, 17
	v_cndmask_b32_e64 v24, v35, v33, s[6:7]
	v_and_b32_e32 v33, 0x7f, v23
	v_bitop3_b32 v35, v23, s8, v23 bitop3:0xc
	v_cmp_gt_i32_e64 s[6:7], 0, v23
	v_readlane_b32 s30, v255, 15
	v_readlane_b32 s81, v255, 41
	v_cndmask_b32_e64 v23, v35, v33, s[6:7]
	v_and_b32_e32 v33, 0x7f, v22
	v_bitop3_b32 v35, v22, s8, v22 bitop3:0xc
	v_cmp_gt_i32_e64 s[6:7], 0, v22
	s_movk_i32 s87, 0x4000
	v_readlane_b32 s93, v255, 36
	v_cndmask_b32_e64 v22, v35, v33, s[6:7]
	v_and_b32_e32 v33, 0x7f, v21
	v_bitop3_b32 v35, v21, s8, v21 bitop3:0xc
	v_cmp_gt_i32_e64 s[6:7], 0, v21
	v_readlane_b32 s89, v255, 30
	v_readlane_b32 s91, v255, 28
	v_cndmask_b32_e64 v21, v35, v33, s[6:7]
	v_and_b32_e32 v33, 0x7f, v20
	v_bitop3_b32 v35, v20, s8, v20 bitop3:0xc
	v_cmp_gt_i32_e64 s[6:7], 0, v20
	v_readlane_b32 s79, v255, 14
	v_readlane_b32 s83, v255, 37
	v_cndmask_b32_e64 v20, v35, v33, s[6:7]
	v_and_b32_e32 v33, 0x7f, v19
	v_bitop3_b32 v35, v19, s8, v19 bitop3:0xc
	v_cmp_gt_i32_e64 s[6:7], 0, v19
	v_readlane_b32 s75, v255, 10
	v_readlane_b32 s85, v255, 38
	v_cndmask_b32_e64 v19, v35, v33, s[6:7]
	v_and_b32_e32 v33, 0x7f, v18
	v_bitop3_b32 v35, v18, s8, v18 bitop3:0xc
	v_cmp_gt_i32_e64 s[6:7], 0, v18
	v_readlane_b32 s77, v255, 12
	v_readlane_b32 s23, v255, 24
	v_cndmask_b32_e64 v18, v35, v33, s[6:7]
	v_and_b32_e32 v33, 0x7f, v17
	v_bitop3_b32 v35, v17, s8, v17 bitop3:0xc
	v_cmp_gt_i32_e64 s[6:7], 0, v17
	s_mov_b32 s18, s36
	s_movk_i32 s27, 0x1200
	v_cndmask_b32_e64 v17, v35, v33, s[6:7]
	v_and_b32_e32 v33, 0x7f, v16
	v_bitop3_b32 v35, v16, s8, v16 bitop3:0xc
	v_cmp_gt_i32_e64 s[6:7], 0, v16
	v_readlane_b32 s35, v255, 18
	v_readlane_b32 s31, v255, 16
	v_cndmask_b32_e64 v33, v35, v33, s[6:7]
	v_lshl_add_u32 v252, v34, 8, v207
	ds_read_b32 v16, v252 offset:4096
	v_bitop3_b32 v35, v15, s8, v15 bitop3:0xc
	s_nop 0
	s_nop 1
	s_nop 1
	s_nop 1
	s_nop 1
	s_nop 1
	s_nop 1
	s_nop 1
	s_nop 1
	s_nop 1
	s_nop 1
	s_nop 1
	s_nop 1
	s_nop 1
	s_nop 1
	v_and_b32_e32 v34, 0x7f, v15
	s_nop 0
	s_waitcnt lgkmcnt(0)
	v_and_b32_e32 v252, 0x7f, v16
	v_cmp_gt_i32_e64 s[6:7], 0, v16
	v_xor_b32_e32 v16, 0x7f, v252
	s_nop 0
	v_cndmask_b32_e64 v16, v16, v252, s[6:7]
	v_cmp_gt_i32_e64 s[6:7], 0, v15
	v_and_b32_e32 v15, 0x7f, v14
	s_nop 0
	v_cndmask_b32_e64 v34, v35, v34, s[6:7]
	v_bitop3_b32 v35, v14, s8, v14 bitop3:0xc
	v_cmp_gt_i32_e64 s[6:7], 0, v14
	v_and_b32_e32 v14, 0x7f, v13
	s_nop 0
	v_cndmask_b32_e64 v35, v35, v15, s[6:7]
	v_bitop3_b32 v15, v13, s8, v13 bitop3:0xc
	v_cmp_gt_i32_e64 s[6:7], 0, v13
	v_and_b32_e32 v13, 0x7f, v12
	s_nop 0
	v_cndmask_b32_e64 v36, v15, v14, s[6:7]
	v_bitop3_b32 v14, v12, s8, v12 bitop3:0xc
	v_cmp_gt_i32_e64 s[6:7], 0, v12
	v_and_b32_e32 v12, 0x7f, v11
	v_max_f32_e32 v15, v59, v60
	v_cndmask_b32_e64 v37, v14, v13, s[6:7]
	v_bitop3_b32 v13, v11, s8, v11 bitop3:0xc
	v_cmp_gt_i32_e64 s[6:7], 0, v11
	v_and_b32_e32 v11, 0x7f, v10
	v_max_f32_e32 v14, v56, v58
	v_cndmask_b32_e64 v38, v13, v12, s[6:7]
	v_bitop3_b32 v12, v10, s8, v10 bitop3:0xc
	v_cmp_gt_i32_e64 s[6:7], 0, v10
	v_and_b32_e32 v10, 0x7f, v9
	v_max_f32_e32 v59, v61, v62
	v_cndmask_b32_e64 v39, v12, v11, s[6:7]
	v_bitop3_b32 v11, v9, s8, v9 bitop3:0xc
	v_cmp_gt_i32_e64 s[6:7], 0, v9
	v_and_b32_e32 v9, 0x7f, v8
	v_max_f32_e32 v60, v63, v173
	v_cndmask_b32_e64 v40, v11, v10, s[6:7]
	v_bitop3_b32 v10, v8, s8, v8 bitop3:0xc
	v_cmp_gt_i32_e64 s[6:7], 0, v8
	v_and_b32_e32 v8, 0x7f, v7
	v_max_f32_e32 v61, v178, v179
	v_cndmask_b32_e64 v41, v10, v9, s[6:7]
	v_bitop3_b32 v9, v7, s8, v7 bitop3:0xc
	v_cmp_gt_i32_e64 s[6:7], 0, v7
	v_and_b32_e32 v7, 0x7f, v6
	v_max_f32_e32 v62, v180, v181
	v_cndmask_b32_e64 v42, v9, v8, s[6:7]
	v_bitop3_b32 v8, v6, s8, v6 bitop3:0xc
	v_cmp_gt_i32_e64 s[6:7], 0, v6
	v_and_b32_e32 v6, 0x7f, v5
	v_max_f32_e32 v9, v210, v211
	v_cndmask_b32_e64 v43, v8, v7, s[6:7]
	v_bitop3_b32 v7, v5, s8, v5 bitop3:0xc
	v_cmp_gt_i32_e64 s[6:7], 0, v5
	v_and_b32_e32 v5, 0x7f, v4
	v_max_f32_e32 v8, v195, v209
	v_cndmask_b32_e64 v44, v7, v6, s[6:7]
	v_bitop3_b32 v6, v4, s8, v4 bitop3:0xc
	v_cmp_gt_i32_e64 s[6:7], 0, v4
	v_and_b32_e32 v4, 0x7f, v3
	v_max_f32_e32 v63, v182, v183
	v_cndmask_b32_e64 v45, v6, v5, s[6:7]
	v_bitop3_b32 v5, v3, s8, v3 bitop3:0xc
	v_cmp_gt_i32_e64 s[6:7], 0, v3
	v_and_b32_e32 v3, 0x7f, v2
	s_nop 0
	v_cndmask_b32_e64 v46, v5, v4, s[6:7]
	v_bitop3_b32 v4, v2, s8, v2 bitop3:0xc
	v_cmp_gt_i32_e64 s[6:7], 0, v2
	v_and_b32_e32 v2, 0x7f, v1
	s_nop 0
	v_cndmask_b32_e64 v47, v4, v3, s[6:7]
	v_bitop3_b32 v3, v1, s8, v1 bitop3:0xc
	v_cmp_gt_i32_e64 s[6:7], 0, v1
	v_and_b32_e32 v1, 0x7f, v0
	v_max_f32_e32 v4, v51, v50
	v_cndmask_b32_e64 v48, v3, v2, s[6:7]
	v_bitop3_b32 v2, v0, s8, v0 bitop3:0xc
	v_cmp_gt_i32_e64 s[6:7], 0, v0
	v_min_f32_e32 v56, v60, v61
	s_nop 0
	v_cndmask_b32_e64 v49, v2, v1, s[6:7]
	v_lshl_add_u32 v252, v214, 8, v207
	ds_read_b32 v0, v252
	v_min_f32_e32 v58, v62, v63
	s_nop 0
	v_max_f32_e32 v60, v60, v61
	v_max_f32_e32 v61, v62, v63
	v_readlane_b32 s46, v255, 21
	v_readlane_b32 s44, v255, 19
	v_readlane_b32 s47, v255, 22
	v_readlane_b32 s45, v255, 20
	s_nop 1
	s_nop 1
	s_nop 1
	s_nop 1
	s_nop 1
	s_nop 1
	s_nop 1
	s_nop 1
	s_nop 1
	s_nop 1
	s_nop 1
	s_nop 1
	s_waitcnt lgkmcnt(0)
	v_and_b32_e32 v252, 0x7f, v0
	v_cmp_gt_i32_e64 s[6:7], 0, v0
	v_xor_b32_e32 v0, 0x7f, v252
	s_nop 0
	v_cndmask_b32_e64 v3, v0, v252, s[6:7]
	v_max_f32_e32 v0, v220, v212
	v_and_b32_e32 v1, 0xff, v0
	v_bitop3_b32 v2, v0, s10, v0 bitop3:0xc
	v_cmp_gt_i32_e64 s[6:7], 0, v0
	v_and_b32_e32 v12, 0xffffff00, v0
	v_lshl_add_u32 v3, v3, 7, v16
	v_cndmask_b32_e64 v0, v2, v1, s[6:7]
	v_lshrrev_b32_e32 v1, 4, v0
	v_lshl_add_u32 v252, v1, 8, v207
	ds_read_b32 v2, v252
	v_and_b32_e32 v0, 15, v0
	s_nop 0
	s_nop 1
	s_nop 1
	s_nop 1
	s_nop 1
	s_nop 1
	s_nop 1
	s_nop 1
	s_nop 1
	s_nop 1
	s_nop 1
	s_nop 1
	s_nop 1
	s_nop 1
	s_nop 1
	s_nop 1
	s_waitcnt lgkmcnt(0)
	v_and_b32_e32 v252, 0x7f, v2
	v_cmp_gt_i32_e64 s[6:7], 0, v2
	v_xor_b32_e32 v2, 0x7f, v252
	s_nop 0
	v_cndmask_b32_e64 v1, v2, v252, s[6:7]
	v_lshl_add_u32 v252, v0, 8, v207
	ds_read_b32 v2, v252 offset:4096
	s_nop 1
	s_nop 1
	s_nop 1
	s_nop 1
	s_nop 1
	s_nop 1
	s_nop 1
	s_nop 1
	s_nop 1
	s_nop 1
	s_nop 1
	s_nop 1
	s_nop 1
	s_nop 1
	s_nop 1
	s_nop 1
	s_waitcnt lgkmcnt(0)
	v_and_b32_e32 v252, 0x7f, v2
	v_cmp_gt_i32_e64 s[6:7], 0, v2
	v_xor_b32_e32 v2, 0x7f, v252
	s_nop 0
	v_cndmask_b32_e64 v0, v2, v252, s[6:7]
	v_lshl_add_u32 v2, v1, 7, v0
	v_max_f32_e32 v0, v216, v215
	v_min_f32_e32 v1, v0, v4
	v_and_b32_e32 v5, 0xff, v1
	v_bitop3_b32 v6, v1, s10, v1 bitop3:0xc
	v_cmp_gt_i32_e64 s[8:9], 0, v1
	v_and_b32_e32 v50, 0xffffff00, v1
	v_max_f32_e32 v0, v0, v4
	v_cndmask_b32_e64 v1, v6, v5, s[8:9]
	v_lshrrev_b32_e32 v5, 4, v1
	v_lshl_add_u32 v252, v5, 8, v207
	ds_read_b32 v6, v252
	v_and_b32_e32 v1, 15, v1
	v_and_b32_e32 v4, 0xff, v0
	v_cmp_gt_i32_e64 s[6:7], 0, v0
	v_and_b32_e32 v51, 0xffffff00, v0
	s_nop 1
	s_nop 1
	s_nop 1
	s_nop 1
	s_nop 1
	s_nop 1
	s_nop 1
	s_nop 1
	s_nop 1
	s_nop 1
	s_nop 1
	s_nop 1
	s_nop 1
	s_nop 1
	s_waitcnt lgkmcnt(0)
	v_and_b32_e32 v252, 0x7f, v6
	v_cmp_gt_i32_e64 s[8:9], 0, v6
	v_xor_b32_e32 v6, 0x7f, v252
	s_nop 0
	v_cndmask_b32_e64 v5, v6, v252, s[8:9]
	v_lshl_add_u32 v252, v1, 8, v207
	ds_read_b32 v6, v252 offset:4096
	s_nop 1
	s_nop 1
	s_nop 1
	s_nop 1
	s_nop 1
	s_nop 1
	s_nop 1
	s_nop 1
	s_nop 1
	s_nop 1
	s_nop 1
	s_nop 1
	s_nop 1
	s_nop 1
	s_nop 1
	s_nop 1
	s_waitcnt lgkmcnt(0)
	v_and_b32_e32 v252, 0x7f, v6
	v_cmp_gt_i32_e64 s[8:9], 0, v6
	v_xor_b32_e32 v6, 0x7f, v252
	s_nop 0
	v_cndmask_b32_e64 v1, v6, v252, s[8:9]
	v_lshl_add_u32 v1, v5, 7, v1
	v_bitop3_b32 v5, v0, s10, v0 bitop3:0xc
	v_cndmask_b32_e64 v0, v5, v4, s[6:7]
	v_lshrrev_b32_e32 v4, 4, v0
	v_lshl_add_u32 v252, v4, 8, v207
	ds_read_b32 v5, v252
	v_and_b32_e32 v0, 15, v0
	s_nop 0
	s_nop 1
	s_nop 1
	s_nop 1
	s_nop 1
	s_nop 1
	s_nop 1
	s_nop 1
	s_nop 1
	s_nop 1
	s_nop 1
	s_nop 1
	s_nop 1
	s_nop 1
	s_nop 1
	s_nop 1
	s_waitcnt lgkmcnt(0)
	v_and_b32_e32 v252, 0x7f, v5
	v_cmp_gt_i32_e64 s[6:7], 0, v5
	v_xor_b32_e32 v5, 0x7f, v252
	s_nop 0
	v_cndmask_b32_e64 v4, v5, v252, s[6:7]
	v_lshl_add_u32 v252, v0, 8, v207
	ds_read_b32 v5, v252 offset:4096
	s_nop 1
	s_nop 1
	s_nop 1
	s_nop 1
	s_nop 1
	s_nop 1
	s_nop 1
	s_nop 1
	s_nop 1
	s_nop 1
	s_nop 1
	s_nop 1
	s_nop 1
	s_nop 1
	s_nop 1
	s_nop 1
	s_waitcnt lgkmcnt(0)
	v_and_b32_e32 v252, 0x7f, v5
	v_cmp_gt_i32_e64 s[6:7], 0, v5
	v_xor_b32_e32 v5, 0x7f, v252
	s_nop 0
	v_cndmask_b32_e64 v0, v5, v252, s[6:7]
	v_lshl_add_u32 v0, v4, 7, v0
	v_max_f32_e32 v4, v52, v190
	v_max_f32_e32 v5, v53, v57
	v_min_f32_e32 v6, v4, v5
	v_min_f32_e32 v10, v8, v9
	v_max_f32_e32 v4, v4, v5
	v_max_f32_e32 v8, v8, v9
	v_min_f32_e32 v7, v6, v10
	v_and_b32_e32 v11, 0xff, v7
	v_bitop3_b32 v13, v7, s10, v7 bitop3:0xc
	v_cmp_gt_i32_e64 s[8:9], 0, v7
	v_and_b32_e32 v52, 0xffffff00, v7
	v_max_f32_e32 v6, v6, v10
	v_cndmask_b32_e64 v7, v13, v11, s[8:9]
	v_lshrrev_b32_e32 v11, 4, v7
	v_lshl_add_u32 v252, v11, 8, v207
	ds_read_b32 v13, v252
	v_and_b32_e32 v7, 15, v7
	v_and_b32_e32 v10, 0xff, v6
	v_cmp_gt_i32_e64 s[6:7], 0, v6
	v_and_b32_e32 v53, 0xffffff00, v6
	s_nop 1
	s_nop 1
	s_nop 1
	s_nop 1
	s_nop 1
	s_nop 1
	s_nop 1
	s_nop 1
	s_nop 1
	s_nop 1
	s_nop 1
	s_nop 1
	s_nop 1
	s_nop 1
	s_waitcnt lgkmcnt(0)
	v_and_b32_e32 v252, 0x7f, v13
	v_cmp_gt_i32_e64 s[8:9], 0, v13
	v_xor_b32_e32 v13, 0x7f, v252
	s_nop 0
	v_cndmask_b32_e64 v11, v13, v252, s[8:9]
	v_lshl_add_u32 v252, v7, 8, v207
	ds_read_b32 v13, v252 offset:4096
	s_nop 1
	s_nop 1
	s_nop 1
	s_nop 1
	s_nop 1
	s_nop 1
	s_nop 1
	s_nop 1
	s_nop 1
	s_nop 1
	s_nop 1
	s_nop 1
	s_nop 1
	s_nop 1
	s_nop 1
	s_nop 1
	s_waitcnt lgkmcnt(0)
	v_and_b32_e32 v252, 0x7f, v13
	v_cmp_gt_i32_e64 s[8:9], 0, v13
	v_xor_b32_e32 v13, 0x7f, v252
	s_nop 0
	v_cndmask_b32_e64 v7, v13, v252, s[8:9]
	v_lshl_add_u32 v7, v11, 7, v7
	v_bitop3_b32 v11, v6, s10, v6 bitop3:0xc
	v_cndmask_b32_e64 v6, v11, v10, s[6:7]
	v_lshrrev_b32_e32 v10, 4, v6
	v_lshl_add_u32 v252, v10, 8, v207
	ds_read_b32 v11, v252
	v_and_b32_e32 v6, 15, v6
	v_max_f32_e32 v13, v54, v55
	v_min_f32_e32 v55, v56, v58
	s_nop 0
	v_max_f32_e32 v58, v56, v58
	s_nop 0
	s_nop 1
	s_nop 1
	s_nop 1
	s_nop 1
	s_nop 1
	s_nop 1
	s_nop 1
	s_nop 1
	s_nop 1
	s_nop 1
	s_nop 1
	s_nop 1
	s_nop 1
	s_waitcnt lgkmcnt(0)
	v_and_b32_e32 v252, 0x7f, v11
	v_cmp_gt_i32_e64 s[6:7], 0, v11
	v_xor_b32_e32 v11, 0x7f, v252
	s_nop 0
	v_cndmask_b32_e64 v10, v11, v252, s[6:7]
	v_lshl_add_u32 v252, v6, 8, v207
	ds_read_b32 v11, v252 offset:4096
	s_nop 1
	s_nop 1
	s_nop 1
	s_nop 1
	s_nop 1
	s_nop 1
	s_nop 1
	s_nop 1
	s_nop 1
	s_nop 1
	s_nop 1
	s_nop 1
	s_nop 1
	s_nop 1
	s_nop 1
	s_nop 1
	s_waitcnt lgkmcnt(0)
	v_and_b32_e32 v252, 0x7f, v11
	v_cmp_gt_i32_e64 s[6:7], 0, v11
	v_xor_b32_e32 v11, 0x7f, v252
	s_nop 0
	v_cndmask_b32_e64 v6, v11, v252, s[6:7]
	v_lshl_add_u32 v6, v10, 7, v6
	v_min_f32_e32 v5, v4, v8
	v_and_b32_e32 v9, 0xff, v5
	v_bitop3_b32 v10, v5, s10, v5 bitop3:0xc
	v_cmp_gt_i32_e64 s[8:9], 0, v5
	v_and_b32_e32 v57, 0xffffff00, v5
	v_max_f32_e32 v4, v4, v8
	v_cndmask_b32_e64 v5, v10, v9, s[8:9]
	v_lshrrev_b32_e32 v9, 4, v5
	v_lshl_add_u32 v252, v9, 8, v207
	ds_read_b32 v10, v252
	v_and_b32_e32 v5, 15, v5
	v_and_b32_e32 v8, 0xff, v4
	v_cmp_gt_i32_e64 s[6:7], 0, v4
	v_and_b32_e32 v209, 0xffffff00, v4
	s_nop 1
	s_nop 1
	s_nop 1
	s_nop 1
	s_nop 1
	s_nop 1
	s_nop 1
	s_nop 1
	s_nop 1
	s_nop 1
	s_nop 1
	s_nop 1
	s_nop 1
	s_nop 1
	s_waitcnt lgkmcnt(0)
	v_and_b32_e32 v252, 0x7f, v10
	v_cmp_gt_i32_e64 s[8:9], 0, v10
	v_xor_b32_e32 v10, 0x7f, v252
	s_nop 0
	v_cndmask_b32_e64 v9, v10, v252, s[8:9]
	v_lshl_add_u32 v252, v5, 8, v207
	ds_read_b32 v10, v252 offset:4096
	s_nop 1
	s_nop 1
	s_nop 1
	s_nop 1
	s_nop 1
	s_nop 1
	s_nop 1
	s_nop 1
	s_nop 1
	s_nop 1
	s_nop 1
	s_nop 1
	s_nop 1
	s_nop 1
	s_nop 1
	s_nop 1
	s_waitcnt lgkmcnt(0)
	v_and_b32_e32 v252, 0x7f, v10
	v_cmp_gt_i32_e64 s[8:9], 0, v10
	v_xor_b32_e32 v10, 0x7f, v252
	s_nop 0
	v_cndmask_b32_e64 v5, v10, v252, s[8:9]
	v_lshl_add_u32 v5, v9, 7, v5
	v_bitop3_b32 v9, v4, s10, v4 bitop3:0xc
	v_cndmask_b32_e64 v4, v9, v8, s[6:7]
	v_lshrrev_b32_e32 v8, 4, v4
	v_lshl_add_u32 v252, v8, 8, v207
	ds_read_b32 v9, v252
	v_and_b32_e32 v4, 15, v4
	s_nop 0
	s_nop 1
	s_nop 1
	s_nop 1
	s_nop 1
	s_nop 1
	s_nop 1
	s_nop 1
	s_nop 1
	s_nop 1
	s_nop 1
	s_nop 1
	s_nop 1
	s_nop 1
	s_nop 1
	s_nop 1
	s_waitcnt lgkmcnt(0)
	v_and_b32_e32 v252, 0x7f, v9
	v_cmp_gt_i32_e64 s[6:7], 0, v9
	v_xor_b32_e32 v9, 0x7f, v252
	s_nop 0
	v_cndmask_b32_e64 v8, v9, v252, s[6:7]
	v_lshl_add_u32 v252, v4, 8, v207
	ds_read_b32 v9, v252 offset:4096
	s_nop 1
	s_nop 1
	s_nop 1
	s_nop 1
	s_nop 1
	s_nop 1
	s_nop 1
	s_nop 1
	s_nop 1
	s_nop 1
	s_nop 1
	s_nop 1
	s_nop 1
	s_nop 1
	s_nop 1
	s_nop 1
	s_waitcnt lgkmcnt(0)
	v_and_b32_e32 v252, 0x7f, v9
	v_cmp_gt_i32_e64 s[6:7], 0, v9
	v_xor_b32_e32 v9, 0x7f, v252
	s_nop 0
	v_cndmask_b32_e64 v4, v9, v252, s[6:7]
	v_lshl_add_u32 v4, v8, 7, v4
	v_min_f32_e32 v8, v13, v14
	v_min_f32_e32 v9, v15, v59
	v_max_f32_e32 v13, v13, v14
	v_max_f32_e32 v59, v15, v59
	v_min_f32_e32 v10, v8, v9
	v_max_f32_e32 v8, v8, v9
	v_min_f32_e32 v11, v10, v55
	v_and_b32_e32 v173, 0xff, v11
	v_bitop3_b32 v178, v11, s10, v11 bitop3:0xc
	v_cmp_gt_i32_e64 s[8:9], 0, v11
	v_and_b32_e32 v54, 0xffffff00, v11
	v_max_f32_e32 v10, v10, v55
	v_cndmask_b32_e64 v11, v178, v173, s[8:9]
	v_lshrrev_b32_e32 v173, 4, v11
	v_lshl_add_u32 v252, v173, 8, v207
	ds_read_b32 v178, v252
	v_and_b32_e32 v11, 15, v11
	v_cmp_gt_i32_e64 s[6:7], 0, v10
	v_and_b32_e32 v55, 0xffffff00, v10
	s_nop 0
	v_min_f32_e32 v14, v13, v59
	v_min_f32_e32 v62, v60, v61
	v_max_f32_e32 v59, v13, v59
	v_max_f32_e32 v60, v60, v61
	s_nop 0
	s_nop 0
	v_min_f32_e32 v13, v59, v60
	v_and_b32_e32 v61, 0xffffff00, v13
	v_max_f32_e32 v59, v59, v60
	v_cmp_gt_i32_e32 vcc, 0, v59
	v_and_b32_e32 v60, 0xffffff00, v59
	v_sub_f32_e32 v12, v12, v60
	v_mul_f32_e32 v12, 0x3fb8aa3b, v12
	s_nop 0
	s_nop 1
	s_nop 1
	s_nop 1
	s_nop 1
	s_nop 1
	s_nop 1
	s_nop 1
	s_waitcnt lgkmcnt(0)
	v_and_b32_e32 v252, 0x7f, v178
	v_cmp_gt_i32_e64 s[8:9], 0, v178
	v_xor_b32_e32 v178, 0x7f, v252
	s_nop 0
	v_cndmask_b32_e64 v173, v178, v252, s[8:9]
	v_lshl_add_u32 v252, v11, 8, v207
	ds_read_b32 v178, v252 offset:4096
	s_nop 1
	s_nop 1
	s_nop 1
	s_nop 1
	s_nop 1
	s_nop 1
	s_nop 1
	s_nop 1
	s_nop 1
	s_nop 1
	s_nop 1
	s_nop 1
	s_nop 1
	s_nop 1
	s_nop 1
	s_nop 1
	s_waitcnt lgkmcnt(0)
	v_and_b32_e32 v252, 0x7f, v178
	v_cmp_gt_i32_e64 s[8:9], 0, v178
	v_xor_b32_e32 v178, 0x7f, v252
	s_nop 0
	v_cndmask_b32_e64 v11, v178, v252, s[8:9]
	v_lshl_add_u32 v11, v173, 7, v11
	v_and_b32_e32 v173, 0xff, v10
	v_bitop3_b32 v178, v10, s10, v10 bitop3:0xc
	v_cndmask_b32_e64 v10, v178, v173, s[6:7]
	v_lshrrev_b32_e32 v173, 4, v10
	v_lshl_add_u32 v252, v173, 8, v207
	ds_read_b32 v178, v252
	v_and_b32_e32 v10, 15, v10
	s_nop 0
	s_nop 1
	s_nop 1
	s_nop 1
	s_nop 1
	s_nop 1
	s_nop 1
	s_nop 1
	s_nop 1
	s_nop 1
	s_nop 1
	s_nop 1
	s_nop 1
	s_nop 1
	s_nop 1
	s_nop 1
	s_waitcnt lgkmcnt(0)
	v_and_b32_e32 v252, 0x7f, v178
	v_cmp_gt_i32_e64 s[6:7], 0, v178
	v_xor_b32_e32 v178, 0x7f, v252
	s_nop 0
	v_cndmask_b32_e64 v173, v178, v252, s[6:7]
	v_lshl_add_u32 v252, v10, 8, v207
	ds_read_b32 v178, v252 offset:4096
	s_nop 1
	s_nop 1
	s_nop 1
	s_nop 1
	s_nop 1
	s_nop 1
	s_nop 1
	s_nop 1
	s_nop 1
	s_nop 1
	s_nop 1
	s_nop 1
	s_nop 1
	s_nop 1
	s_nop 1
	s_nop 1
	s_waitcnt lgkmcnt(0)
	v_and_b32_e32 v252, 0x7f, v178
	v_cmp_gt_i32_e64 s[6:7], 0, v178
	v_xor_b32_e32 v178, 0x7f, v252
	s_nop 0
	v_cndmask_b32_e64 v10, v178, v252, s[6:7]
	v_lshl_add_u32 v10, v173, 7, v10
	v_min_f32_e32 v9, v8, v58
	v_and_b32_e32 v173, 0xff, v9
	v_bitop3_b32 v178, v9, s10, v9 bitop3:0xc
	v_cmp_gt_i32_e64 s[8:9], 0, v9
	v_and_b32_e32 v56, 0xffffff00, v9
	v_max_f32_e32 v8, v8, v58
	v_cndmask_b32_e64 v9, v178, v173, s[8:9]
	v_lshrrev_b32_e32 v173, 4, v9
	v_lshl_add_u32 v252, v173, 8, v207
	ds_read_b32 v178, v252
	v_and_b32_e32 v9, 15, v9
	v_cmp_gt_i32_e64 s[6:7], 0, v8
	v_and_b32_e32 v58, 0xffffff00, v8
	s_nop 0
	s_nop 1
	s_nop 1
	s_nop 1
	s_nop 1
	s_nop 1
	s_nop 1
	s_nop 1
	s_nop 1
	s_nop 1
	s_nop 1
	s_nop 1
	s_nop 1
	s_nop 1
	s_nop 1
	s_waitcnt lgkmcnt(0)
	v_and_b32_e32 v252, 0x7f, v178
	v_cmp_gt_i32_e64 s[8:9], 0, v178
	v_xor_b32_e32 v178, 0x7f, v252
	s_nop 0
	v_cndmask_b32_e64 v173, v178, v252, s[8:9]
	v_lshl_add_u32 v252, v9, 8, v207
	ds_read_b32 v178, v252 offset:4096
	s_nop 1
	s_nop 1
	s_nop 1
	s_nop 1
	s_nop 1
	s_nop 1
	s_nop 1
	s_nop 1
	s_nop 1
	s_nop 1
	s_nop 1
	s_nop 1
	s_nop 1
	s_nop 1
	s_nop 1
	s_nop 1
	s_waitcnt lgkmcnt(0)
	v_and_b32_e32 v252, 0x7f, v178
	v_cmp_gt_i32_e64 s[8:9], 0, v178
	v_xor_b32_e32 v178, 0x7f, v252
	s_nop 0
	v_cndmask_b32_e64 v9, v178, v252, s[8:9]
	v_lshl_add_u32 v9, v173, 7, v9
	v_and_b32_e32 v173, 0xff, v8
	v_bitop3_b32 v178, v8, s10, v8 bitop3:0xc
	v_cndmask_b32_e64 v8, v178, v173, s[6:7]
	v_lshrrev_b32_e32 v173, 4, v8
	v_lshl_add_u32 v252, v173, 8, v207
	ds_read_b32 v178, v252
	v_and_b32_e32 v8, 15, v8
	s_nop 0
	s_nop 1
	s_nop 1
	s_nop 1
	s_nop 1
	s_nop 1
	s_nop 1
	s_nop 1
	s_nop 1
	s_nop 1
	s_nop 1
	s_nop 1
	s_nop 1
	s_nop 1
	s_nop 1
	s_nop 1
	s_waitcnt lgkmcnt(0)
	v_and_b32_e32 v252, 0x7f, v178
	v_cmp_gt_i32_e64 s[6:7], 0, v178
	v_xor_b32_e32 v178, 0x7f, v252
	s_nop 0
	v_cndmask_b32_e64 v173, v178, v252, s[6:7]
	v_lshl_add_u32 v252, v8, 8, v207
	ds_read_b32 v178, v252 offset:4096
	s_nop 1
	s_nop 1
	s_nop 1
	s_nop 1
	s_nop 1
	s_nop 1
	s_nop 1
	s_nop 1
	s_nop 1
	s_nop 1
	s_nop 1
	s_nop 1
	s_nop 1
	s_nop 1
	s_nop 1
	s_nop 1
	s_waitcnt lgkmcnt(0)
	v_and_b32_e32 v252, 0x7f, v178
	v_cmp_gt_i32_e64 s[6:7], 0, v178
	v_xor_b32_e32 v178, 0x7f, v252
	s_nop 0
	v_cndmask_b32_e64 v8, v178, v252, s[6:7]
	v_lshl_add_u32 v8, v173, 7, v8
	v_min_f32_e32 v15, v14, v62
	v_and_b32_e32 v173, 0xff, v15
	v_bitop3_b32 v178, v15, s10, v15 bitop3:0xc
	v_cmp_gt_i32_e64 s[8:9], 0, v15
	v_and_b32_e32 v63, 0xffffff00, v15
	v_max_f32_e32 v14, v14, v62
	v_cndmask_b32_e64 v15, v178, v173, s[8:9]
	v_lshrrev_b32_e32 v173, 4, v15
	v_lshl_add_u32 v252, v173, 8, v207
	ds_read_b32 v178, v252
	v_and_b32_e32 v15, 15, v15
	v_cmp_gt_i32_e64 s[6:7], 0, v14
	v_and_b32_e32 v62, 0xffffff00, v14
	s_nop 0
	s_nop 1
	s_nop 1
	s_nop 1
	s_nop 1
	s_nop 1
	s_nop 1
	s_nop 1
	s_nop 1
	s_nop 1
	s_nop 1
	s_nop 1
	s_nop 1
	s_nop 1
	s_nop 1
	s_waitcnt lgkmcnt(0)
	v_and_b32_e32 v252, 0x7f, v178
	v_cmp_gt_i32_e64 s[8:9], 0, v178
	v_xor_b32_e32 v178, 0x7f, v252
	s_nop 0
	v_cndmask_b32_e64 v173, v178, v252, s[8:9]
	v_lshl_add_u32 v252, v15, 8, v207
	ds_read_b32 v178, v252 offset:4096
	s_nop 1
	s_nop 1
	s_nop 1
	s_nop 1
	s_nop 1
	s_nop 1
	s_nop 1
	s_nop 1
	s_nop 1
	s_nop 1
	s_nop 1
	s_nop 1
	s_nop 1
	s_nop 1
	s_nop 1
	s_nop 1
	s_waitcnt lgkmcnt(0)
	v_and_b32_e32 v252, 0x7f, v178
	v_cmp_gt_i32_e64 s[8:9], 0, v178
	v_xor_b32_e32 v178, 0x7f, v252
	s_nop 0
	v_cndmask_b32_e64 v15, v178, v252, s[8:9]
	v_lshl_add_u32 v15, v173, 7, v15
	v_and_b32_e32 v173, 0xff, v14
	v_bitop3_b32 v178, v14, s10, v14 bitop3:0xc
	v_cndmask_b32_e64 v14, v178, v173, s[6:7]
	v_lshrrev_b32_e32 v173, 4, v14
	v_lshl_add_u32 v252, v173, 8, v207
	ds_read_b32 v178, v252
	v_and_b32_e32 v14, 15, v14
	v_readlane_b32 s8, v253, 23
	v_readlane_b32 s9, v253, 24
	s_nop 0
	s_nop 1
	s_nop 1
	s_nop 1
	s_nop 1
	s_nop 1
	s_nop 1
	s_nop 1
	s_nop 1
	s_nop 1
	s_nop 1
	s_nop 1
	s_nop 1
	s_nop 1
	s_nop 1
	s_waitcnt lgkmcnt(0)
	v_and_b32_e32 v252, 0x7f, v178
	v_cmp_gt_i32_e64 s[6:7], 0, v178
	v_xor_b32_e32 v178, 0x7f, v252
	s_nop 0
	v_cndmask_b32_e64 v173, v178, v252, s[6:7]
	v_lshl_add_u32 v252, v14, 8, v207
	ds_read_b32 v178, v252 offset:4096
	s_nop 1
	s_nop 1
	s_nop 1
	s_nop 1
	s_nop 1
	s_nop 1
	s_nop 1
	s_nop 1
	s_nop 1
	s_nop 1
	s_nop 1
	s_nop 1
	s_nop 1
	s_nop 1
	s_nop 1
	s_nop 1
	s_waitcnt lgkmcnt(0)
	v_and_b32_e32 v252, 0x7f, v178
	v_cmp_gt_i32_e64 s[6:7], 0, v178
	v_xor_b32_e32 v178, 0x7f, v252
	s_nop 0
	v_cndmask_b32_e64 v14, v178, v252, s[6:7]
	v_lshl_add_u32 v14, v173, 7, v14
	v_and_b32_e32 v173, 0xff, v13
	v_bitop3_b32 v178, v13, s10, v13 bitop3:0xc
	v_cmp_gt_i32_e64 s[6:7], 0, v13
	s_nop 1
	v_cndmask_b32_e64 v13, v178, v173, s[6:7]
	v_lshrrev_b32_e32 v173, 4, v13
	v_lshl_add_u32 v252, v173, 8, v207
	ds_read_b32 v178, v252
	v_and_b32_e32 v13, 15, v13
	s_nop 0
	s_nop 1
	s_nop 1
	s_nop 1
	s_nop 1
	s_nop 1
	s_nop 1
	s_nop 1
	s_nop 1
	s_nop 1
	s_nop 1
	s_nop 1
	s_nop 1
	s_nop 1
	s_nop 1
	s_nop 1
	s_waitcnt lgkmcnt(0)
	v_and_b32_e32 v252, 0x7f, v178
	v_cmp_gt_i32_e64 s[6:7], 0, v178
	v_xor_b32_e32 v178, 0x7f, v252
	s_nop 0
	v_cndmask_b32_e64 v173, v178, v252, s[6:7]
	v_lshl_add_u32 v252, v13, 8, v207
	ds_read_b32 v178, v252 offset:4096
	s_nop 1
	s_nop 1
	s_nop 1
	s_nop 1
	s_nop 1
	s_nop 1
	s_nop 1
	s_nop 1
	s_nop 1
	s_nop 1
	s_nop 1
	s_nop 1
	s_nop 1
	s_nop 1
	s_nop 1
	s_nop 1
	s_waitcnt lgkmcnt(0)
	v_and_b32_e32 v252, 0x7f, v178
	v_cmp_gt_i32_e64 s[6:7], 0, v178
	v_xor_b32_e32 v178, 0x7f, v252
	s_nop 0
	v_cndmask_b32_e64 v13, v178, v252, s[6:7]
	v_lshl_add_u32 v13, v173, 7, v13
	v_and_b32_e32 v173, 0xff, v59
	v_bitop3_b32 v178, v59, s10, v59 bitop3:0xc
	v_cndmask_b32_e32 v59, v178, v173, vcc
	v_lshrrev_b32_e32 v173, 4, v59
	v_cmp_gt_u32_e32 vcc, 16, v59
	s_nop 1
	v_cndmask_b32_e32 v49, 0, v49, vcc
	v_cmp_eq_u32_e32 vcc, 1, v173
	s_nop 1
	v_cndmask_b32_e32 v48, v49, v48, vcc
	v_cmp_eq_u32_e32 vcc, 2, v173
	s_nop 1
	v_cndmask_b32_e32 v47, v48, v47, vcc
	v_cmp_eq_u32_e32 vcc, 3, v173
	s_nop 1
	v_cndmask_b32_e32 v46, v47, v46, vcc
	v_cmp_eq_u32_e32 vcc, 4, v173
	s_nop 1
	v_cndmask_b32_e32 v45, v46, v45, vcc
	v_cmp_eq_u32_e32 vcc, 5, v173
	s_nop 1
	v_cndmask_b32_e32 v44, v45, v44, vcc
	v_cmp_eq_u32_e32 vcc, 6, v173
	s_nop 1
	v_cndmask_b32_e32 v43, v44, v43, vcc
	v_cmp_eq_u32_e32 vcc, 7, v173
	s_nop 1
	v_cndmask_b32_e32 v42, v43, v42, vcc
	v_cmp_eq_u32_e32 vcc, 8, v173
	s_nop 1
	v_cndmask_b32_e32 v41, v42, v41, vcc
	v_cmp_eq_u32_e32 vcc, 9, v173
	s_nop 1
	v_cndmask_b32_e32 v40, v41, v40, vcc
	v_cmp_eq_u32_e32 vcc, 10, v173
	s_nop 1
	v_cndmask_b32_e32 v39, v40, v39, vcc
	v_cmp_eq_u32_e32 vcc, 11, v173
	s_nop 1
	v_cndmask_b32_e32 v38, v39, v38, vcc
	v_cmp_eq_u32_e32 vcc, 12, v173
	v_and_b32_e32 v39, 15, v59
	s_nop 0
	v_cndmask_b32_e32 v37, v38, v37, vcc
	v_cmp_eq_u32_e32 vcc, 13, v173
	s_nop 1
	v_cndmask_b32_e32 v36, v37, v36, vcc
	v_cmp_eq_u32_e32 vcc, 14, v173
	s_nop 1
	v_cndmask_b32_e32 v35, v36, v35, vcc
	v_cmp_eq_u32_e32 vcc, 15, v173
	v_exp_f32_e32 v36, v12
	v_and_b32_e32 v12, 0xffffff00, v32
	v_cndmask_b32_e32 v38, v35, v34, vcc
	v_cmp_eq_u32_e32 vcc, 0, v39
	v_sub_f32_e32 v12, v12, v60
	v_mul_f32_e32 v12, 0x3fb8aa3b, v12
	v_cndmask_b32_e32 v33, 0, v33, vcc
	v_cmp_eq_u32_e32 vcc, 1, v39
	v_exp_f32_e32 v37, v12
	s_nop 0
	v_cndmask_b32_e32 v17, v33, v17, vcc
	v_cmp_eq_u32_e32 vcc, 2, v39
	v_sub_f32_e32 v33, v51, v60
	v_mul_f32_e32 v33, 0x3fb8aa3b, v33
	v_cndmask_b32_e32 v17, v17, v18, vcc
	v_cmp_eq_u32_e32 vcc, 3, v39
	v_sub_f32_e32 v18, v60, v60
	v_mul_f32_e32 v18, 0x3fb8aa3b, v18
	v_cndmask_b32_e32 v17, v17, v19, vcc
	v_cmp_eq_u32_e32 vcc, 4, v39
	v_sub_f32_e32 v19, v61, v60
	v_exp_f32_e32 v18, v18
	v_cndmask_b32_e32 v17, v17, v20, vcc
	v_cmp_eq_u32_e32 vcc, 5, v39
	v_mul_f32_e32 v19, 0x3fb8aa3b, v19
	v_sub_f32_e32 v20, v62, v60
	v_cndmask_b32_e32 v17, v17, v21, vcc
	v_exp_f32_e32 v19, v19
	v_mul_f32_e32 v20, 0x3fb8aa3b, v20
	v_sub_f32_e32 v21, v63, v60
	v_cmp_eq_u32_e32 vcc, 6, v39
	v_exp_f32_e32 v20, v20
	v_mul_f32_e32 v21, 0x3fb8aa3b, v21
	v_cndmask_b32_e32 v17, v17, v22, vcc
	v_cmp_eq_u32_e32 vcc, 7, v39
	v_exp_f32_e32 v21, v21
	v_add_f32_e32 v22, 0, v18
	v_cndmask_b32_e32 v17, v17, v23, vcc
	v_cmp_eq_u32_e32 vcc, 8, v39
	v_add_f32_e32 v22, v19, v22
	v_add_f32_e32 v22, v20, v22
	v_cndmask_b32_e32 v17, v17, v24, vcc
	v_cmp_eq_u32_e32 vcc, 9, v39
	v_sub_f32_e32 v23, v56, v60
	v_mul_f32_e32 v23, 0x3fb8aa3b, v23
	v_cndmask_b32_e32 v17, v17, v25, vcc
	v_cmp_eq_u32_e32 vcc, 10, v39
	v_sub_f32_e32 v24, v55, v60
	v_exp_f32_e32 v23, v23
	v_cndmask_b32_e32 v17, v17, v26, vcc
	v_add_f32_e32 v26, v21, v22
	v_sub_f32_e32 v22, v58, v60
	v_mul_f32_e32 v22, 0x3fb8aa3b, v22
	v_exp_f32_e32 v22, v22
	v_mul_f32_e32 v24, 0x3fb8aa3b, v24
	v_sub_f32_e32 v25, v54, v60
	v_exp_f32_e32 v24, v24
	v_mul_f32_e32 v25, 0x3fb8aa3b, v25
	v_cmp_eq_u32_e32 vcc, 11, v39
	v_exp_f32_e32 v25, v25
	v_add_f32_e32 v26, v22, v26
	v_cndmask_b32_e32 v17, v17, v27, vcc
	v_cmp_eq_u32_e32 vcc, 12, v39
	v_add_f32_e32 v26, v23, v26
	v_add_f32_e32 v26, v24, v26
	v_cndmask_b32_e32 v17, v17, v28, vcc
	v_cmp_eq_u32_e32 vcc, 13, v39
	v_sub_f32_e32 v27, v57, v60
	v_mul_f32_e32 v27, 0x3fb8aa3b, v27
	v_cndmask_b32_e32 v17, v17, v29, vcc
	v_cmp_eq_u32_e32 vcc, 14, v39
	v_sub_f32_e32 v28, v53, v60
	v_exp_f32_e32 v27, v27
	v_cndmask_b32_e32 v17, v17, v30, vcc
	v_add_f32_e32 v30, v25, v26
	v_sub_f32_e32 v26, v209, v60
	v_mul_f32_e32 v26, 0x3fb8aa3b, v26
	v_exp_f32_e32 v26, v26
	v_mul_f32_e32 v28, 0x3fb8aa3b, v28
	v_sub_f32_e32 v29, v52, v60
	v_exp_f32_e32 v28, v28
	v_mul_f32_e32 v29, 0x3fb8aa3b, v29
	v_exp_f32_e32 v29, v29
	v_exp_f32_e32 v34, v33
	v_sub_f32_e32 v33, v50, v60
	v_add_f32_e32 v30, v26, v30
	v_mul_f32_e32 v33, 0x3fb8aa3b, v33
	v_add_f32_e32 v30, v27, v30
	v_exp_f32_e32 v35, v33
	v_add_f32_e32 v30, v28, v30
	v_add_f32_e32 v30, v29, v30
	v_add_f32_e32 v12, v34, v30
	v_add_f32_e32 v12, v35, v12
	v_add_f32_e32 v12, v36, v12
	v_add_f32_e32 v30, v37, v12
	v_div_scale_f32 v32, s[6:7], v30, v30, 1.0
	v_rcp_f32_e32 v33, v32
	v_cmp_eq_u32_e32 vcc, 15, v39
	v_readlane_b32 s6, v255, 46
	s_lshl_b32 s6, s6, 4
	v_cndmask_b32_e32 v12, v17, v31, vcc
	v_fma_f32 v17, -v32, v33, 1.0
	v_fmac_f32_e32 v33, v17, v33
	v_div_scale_f32 v17, vcc, 1.0, v30, 1.0
	v_mul_f32_e32 v31, v17, v33
	v_lshl_add_u32 v12, v38, 7, v12
	v_fma_f32 v38, -v32, v31, v17
	v_fmac_f32_e32 v31, v38, v33
	v_fma_f32 v17, -v32, v31, v17
	v_div_fmas_f32 v17, v17, v33, v31
	v_div_fixup_f32 v30, v17, v30, 1.0
	v_lshlrev_b64 v[16:17], 9, v[176:177]
	s_ashr_i32 s7, s6, 31
	v_lshl_add_u64 v[32:33], s[94:95], 0, v[16:17]
	s_lshl_b64 s[6:7], s[6:7], 2
	v_lshl_add_u64 v[32:33], v[32:33], 0, s[6:7]
	v_lshl_add_u64 v[16:17], s[8:9], 0, v[16:17]
	v_lshl_add_u64 v[16:17], v[16:17], 0, s[6:7]
	global_store_dwordx4 v[32:33], v[12:15], off
	v_readlane_b32 s8, v255, 44
	v_readlane_b32 s9, v255, 45
	v_pk_mul_f32 v[12:13], v[18:19], v[30:31] op_sel_hi:[1,0]
	v_pk_mul_f32 v[14:15], v[20:21], v[30:31] op_sel_hi:[1,0]
	global_store_dwordx4 v[16:17], v[12:15], off
	global_store_dwordx4 v[32:33], v[8:11], off offset:16
	s_nop 1
	v_pk_mul_f32 v[8:9], v[22:23], v[30:31] op_sel_hi:[1,0]
	v_pk_mul_f32 v[10:11], v[24:25], v[30:31] op_sel_hi:[1,0]
	global_store_dwordx4 v[16:17], v[8:11], off offset:16
	global_store_dwordx4 v[32:33], v[4:7], off offset:32
	s_nop 1
	v_pk_mul_f32 v[4:5], v[26:27], v[30:31] op_sel_hi:[1,0]
	v_pk_mul_f32 v[6:7], v[28:29], v[30:31] op_sel_hi:[1,0]
	global_store_dwordx4 v[16:17], v[4:7], off offset:32
	global_store_dwordx4 v[32:33], v[0:3], off offset:48
	s_nop 1
	v_pk_mul_f32 v[0:1], v[34:35], v[30:31] op_sel_hi:[1,0]
	v_pk_mul_f32 v[2:3], v[36:37], v[30:31] op_sel_hi:[1,0]
	global_store_dwordx4 v[16:17], v[0:3], off offset:48
	s_branch .LBB0_696
